# speedup vs baseline: 1.1310x; 1.1310x over previous
_Z8attn_fwdPKfPKiPf:
	s_load_dwordx4 s[4:7], s[0:1], 0x0
	s_load_dwordx2 s[12:13], s[0:1], 0x10
	v_and_b32_e32 v235, 63, v0
	v_lshrrev_b32_e32 v236, 4, v0
	v_and_b32_e32 v237, 15, v0
	v_readfirstlane_b32 s17, v0
	s_nop 3
	s_lshr_b32 s17, s17, 6
	v_mul_u32_u24_e32 v229, 0x3000, v236
	v_lshl_add_u32 v229, v237, 4, v229
	v_mul_u32_u24_e32 v227, 144, v236
	v_lshl_add_u32 v227, v237, 3, v227
	v_lshlrev_b32_e32 v230, 2, v235
	v_and_b32_e32 v238, 31, v0
	v_bfe_u32 v236, v0, 5, 1
	v_mul_u32_u24_e32 v225, 144, v238
	v_lshl_add_u32 v225, v236, 4, v225
	v_add_u32_e32 v226, 36864, v225
	v_lshlrev_b32_e32 v234, 2, v236
	v_mul_u32_u24_e32 v228, 144, v235
	s_lshl_b32 s31, s17, 4
	s_add_u32 s31, s31, 36864
	v_add_u32_e32 v228, s31, v228
	s_mul_i32 s32, s17, 8704
	s_add_u32 s32, s32, 73728
	v_lshrrev_b32_e32 v231, 4, v235
	v_mul_u32_u24_e32 v239, 144, v231
	v_lshl_add_u32 v239, v237, 3, v239
	v_add_u32_e32 v239, s32, v239
	v_add_u32_e32 v240, s32, v225
	v_mul_u32_u24_e32 v241, 272, v238
	v_lshl_add_u32 v241, v236, 4, v241
	v_add_u32_e32 v241, s32, v241
	v_mul_u32_u24_e32 v242, 272, v231
	v_lshl_add_u32 v242, v237, 4, v242
	v_add_u32_e32 v242, s32, v242
	v_mul_u32_u24_e32 v243, 0x3000, v231
	v_lshl_add_u32 v243, v237, 4, v243
	v_lshlrev_b32_e32 v244, 12, v231
	v_lshl_add_u32 v244, v237, 4, v244
	s_and_b32 s33, s2, 7
	s_lshr_b32 s31, s2, 3
	s_and_b32 s39, s31, 3
	s_lshr_b32 s40, s31, 3
	s_lshr_b32 s41, s31, 2
	s_and_b32 s41, s41, 1
	s_lshl_b32 s33, s33, 1
	s_add_u32 s41, s41, s33
	s_mul_i32 s16, s40, 0x1800000
	s_lshl_b32 s31, s41, 8
	s_add_u32 s16, s16, s31
	s_add_u32 s18, s16, 4096
	s_lshr_b32 s31, s17, 1
	s_lshl_b32 s31, s31, 4
	s_and_b32 s33, s17, 1
	s_lshl_b32 s33, s33, 2
	s_add_u32 s31, s31, s33
	s_mul_i32 s31, s31, 0x3000
	s_add_u32 s19, s16, 8192
	s_add_u32 s19, s19, s31
	s_lshl_b32 s22, s40, 13
	s_lshl_b32 s31, s39, 8
	s_lshl_b32 s33, s17, 5
	s_add_u32 s31, s31, s33
	s_mul_i32 s29, s31, 0x3000
	s_add_u32 s29, s29, s16
	s_lshl_b32 s33, s40, 11
	s_add_u32 s31, s31, s33
	s_lshl_b32 s30, s31, 12
	s_lshl_b32 s31, s41, 8
	s_add_u32 s30, s30, s31
	s_mov_b32 s37, 0x46800000
	s_mov_b32 s38, 0xbf800000
	s_mov_b32 s34, 0x46800000
	s_mov_b32 s35, 0xc6616bcd
	s_mov_b32 s36, 0x3e38aa3b
	s_mov_b32 s23, 0
	s_mov_b32 s27, 0
	s_waitcnt lgkmcnt(0)
	s_mov_b32 s8, s6
	s_and_b32 s9, s7, 0xffff
	s_mov_b32 s10, 0x7fffffff
	s_mov_b32 s11, 0x20000
	s_and_b32 s5, s5, 0xffff
	s_mov_b32 s6, 0x7fffffff
	s_mov_b32 s7, 0x20000
	s_and_b32 s13, s13, 0xffff
	s_mov_b32 s14, 0x7fffffff
	s_mov_b32 s15, 0x20000
	s_add_u32 s31, s18, 0x0
	buffer_load_dwordx4 v[64:67], v229, s[4:7], s31 offen
	s_add_u32 s31, s18, 0x60000
	buffer_load_dwordx4 v[68:71], v229, s[4:7], s31 offen
	s_add_u32 s31, s18, 0xc0000
	buffer_load_dwordx4 v[72:75], v229, s[4:7], s31 offen
	s_add_u32 s31, s18, 0x120000
	buffer_load_dwordx4 v[76:79], v229, s[4:7], s31 offen
	s_add_u32 s31, s19, 0x0
	buffer_load_dword v80, v230, s[4:7], s31 offen
	s_add_u32 s31, s19, 0x3000
	buffer_load_dword v81, v230, s[4:7], s31 offen
	s_add_u32 s31, s19, 0x6000
	buffer_load_dword v82, v230, s[4:7], s31 offen
	s_add_u32 s31, s19, 0x9000
	buffer_load_dword v83, v230, s[4:7], s31 offen
	s_add_u32 s31, s19, 0x18000
	buffer_load_dword v84, v230, s[4:7], s31 offen
	s_add_u32 s31, s19, 0x1b000
	buffer_load_dword v85, v230, s[4:7], s31 offen
	s_add_u32 s31, s19, 0x1e000
	buffer_load_dword v86, v230, s[4:7], s31 offen
	s_add_u32 s31, s19, 0x21000
	buffer_load_dword v87, v230, s[4:7], s31 offen
	s_add_u32 s31, s19, 0xc0000
	buffer_load_dword v88, v230, s[4:7], s31 offen
	s_add_u32 s31, s19, 0xc3000
	buffer_load_dword v89, v230, s[4:7], s31 offen
	s_add_u32 s31, s19, 0xc6000
	buffer_load_dword v90, v230, s[4:7], s31 offen
	s_add_u32 s31, s19, 0xc9000
	buffer_load_dword v91, v230, s[4:7], s31 offen
	s_add_u32 s31, s19, 0xd8000
	buffer_load_dword v92, v230, s[4:7], s31 offen
	s_add_u32 s31, s19, 0xdb000
	buffer_load_dword v93, v230, s[4:7], s31 offen
	s_add_u32 s31, s19, 0xde000
	buffer_load_dword v94, v230, s[4:7], s31 offen
	s_add_u32 s31, s19, 0xe1000
	buffer_load_dword v95, v230, s[4:7], s31 offen
	buffer_load_dword v224, v230, s[8:11], s22 offen
	s_add_u32 s31, s29, 0x0
	buffer_load_dwordx4 v[0:3], v243, s[4:7], s31 offen nt
	s_add_u32 s31, s29, 0xc000
	buffer_load_dwordx4 v[4:7], v243, s[4:7], s31 offen nt
	s_add_u32 s31, s29, 0x18000
	buffer_load_dwordx4 v[8:11], v243, s[4:7], s31 offen nt
	s_add_u32 s31, s29, 0x24000
	buffer_load_dwordx4 v[12:15], v243, s[4:7], s31 offen nt
	s_add_u32 s31, s29, 0x30000
	buffer_load_dwordx4 v[16:19], v243, s[4:7], s31 offen nt
	s_add_u32 s31, s29, 0x3c000
	buffer_load_dwordx4 v[20:23], v243, s[4:7], s31 offen nt
	s_add_u32 s31, s29, 0x48000
	buffer_load_dwordx4 v[24:27], v243, s[4:7], s31 offen nt
	s_add_u32 s31, s29, 0x54000
	buffer_load_dwordx4 v[28:31], v243, s[4:7], s31 offen nt
	s_add_u32 s31, s29, 0xc00000
	buffer_load_dwordx4 v[32:35], v243, s[4:7], s31 offen nt
	s_add_u32 s31, s29, 0xc0c000
	buffer_load_dwordx4 v[36:39], v243, s[4:7], s31 offen nt
	s_add_u32 s31, s29, 0xc18000
	buffer_load_dwordx4 v[40:43], v243, s[4:7], s31 offen nt
	s_add_u32 s31, s29, 0xc24000
	buffer_load_dwordx4 v[44:47], v243, s[4:7], s31 offen nt
	s_add_u32 s31, s29, 0xc30000
	buffer_load_dwordx4 v[48:51], v243, s[4:7], s31 offen nt
	s_add_u32 s31, s29, 0xc3c000
	buffer_load_dwordx4 v[52:55], v243, s[4:7], s31 offen nt
	s_add_u32 s31, s29, 0xc48000
	buffer_load_dwordx4 v[56:59], v243, s[4:7], s31 offen nt
	s_add_u32 s31, s29, 0xc54000
	buffer_load_dwordx4 v[60:63], v243, s[4:7], s31 offen nt
	s_waitcnt vmcnt(16)
	v_cvt_pk_f16_f32 v64, v64, v65
	v_cvt_pk_f16_f32 v65, v66, v67
	ds_write_b64 v227, v[64:65] offset:0
	v_cvt_pk_f16_f32 v68, v68, v69
	v_cvt_pk_f16_f32 v69, v70, v71
	ds_write_b64 v227, v[68:69] offset:4608
	v_cvt_pk_f16_f32 v72, v72, v73
	v_cvt_pk_f16_f32 v73, v74, v75
	ds_write_b64 v227, v[72:73] offset:9216
	v_cvt_pk_f16_f32 v76, v76, v77
	v_cvt_pk_f16_f32 v77, v78, v79
	ds_write_b64 v227, v[76:77] offset:13824
	v_cvt_pk_f16_f32 v80, v80, v81
	v_cvt_pk_f16_f32 v81, v82, v83
	v_cvt_pk_f16_f32 v82, v84, v85
	v_cvt_pk_f16_f32 v83, v86, v87
	ds_write_b128 v228, v[80:83] offset:0
	v_cvt_pk_f16_f32 v88, v88, v89
	v_cvt_pk_f16_f32 v89, v90, v91
	v_cvt_pk_f16_f32 v90, v92, v93
	v_cvt_pk_f16_f32 v91, v94, v95
	ds_write_b128 v228, v[88:91] offset:9216
	s_add_u32 s31, s18, 0x180000
	buffer_load_dwordx4 v[208:211], v229, s[4:7], s31 offen
	s_add_u32 s31, s18, 0x1e0000
	buffer_load_dwordx4 v[212:215], v229, s[4:7], s31 offen
	s_add_u32 s31, s19, 0x180000
	buffer_load_dword v216, v230, s[4:7], s31 offen
	s_add_u32 s31, s19, 0x183000
	buffer_load_dword v217, v230, s[4:7], s31 offen
	s_add_u32 s31, s19, 0x186000
	buffer_load_dword v218, v230, s[4:7], s31 offen
	s_add_u32 s31, s19, 0x189000
	buffer_load_dword v219, v230, s[4:7], s31 offen
	s_add_u32 s31, s19, 0x198000
	buffer_load_dword v220, v230, s[4:7], s31 offen
	s_add_u32 s31, s19, 0x19b000
	buffer_load_dword v221, v230, s[4:7], s31 offen
	s_add_u32 s31, s19, 0x19e000
	buffer_load_dword v222, v230, s[4:7], s31 offen
	s_add_u32 s31, s19, 0x1a1000
	buffer_load_dword v223, v230, s[4:7], s31 offen
	s_waitcnt vmcnt(10)
	v_mul_f32_e32 v0, s36, v0
	v_mul_f32_e32 v1, s36, v1
	v_mul_f32_e32 v2, s36, v2
	v_mul_f32_e32 v3, s36, v3
	v_cvt_pk_f16_f32 v0, v0, v1
	v_cvt_pk_f16_f32 v1, v2, v3
	ds_write_b64 v239, v[0:1] offset:0
	v_mul_f32_e32 v4, s36, v4
	v_mul_f32_e32 v5, s36, v5
	v_mul_f32_e32 v6, s36, v6
	v_mul_f32_e32 v7, s36, v7
	v_cvt_pk_f16_f32 v4, v4, v5
	v_cvt_pk_f16_f32 v5, v6, v7
	ds_write_b64 v239, v[4:5] offset:576
	v_mul_f32_e32 v8, s36, v8
	v_mul_f32_e32 v9, s36, v9
	v_mul_f32_e32 v10, s36, v10
	v_mul_f32_e32 v11, s36, v11
	v_cvt_pk_f16_f32 v8, v8, v9
	v_cvt_pk_f16_f32 v9, v10, v11
	ds_write_b64 v239, v[8:9] offset:1152
	v_mul_f32_e32 v12, s36, v12
	v_mul_f32_e32 v13, s36, v13
	v_mul_f32_e32 v14, s36, v14
	v_mul_f32_e32 v15, s36, v15
	v_cvt_pk_f16_f32 v12, v12, v13
	v_cvt_pk_f16_f32 v13, v14, v15
	ds_write_b64 v239, v[12:13] offset:1728
	v_mul_f32_e32 v16, s36, v16
	v_mul_f32_e32 v17, s36, v17
	v_mul_f32_e32 v18, s36, v18
	v_mul_f32_e32 v19, s36, v19
	v_cvt_pk_f16_f32 v16, v16, v17
	v_cvt_pk_f16_f32 v17, v18, v19
	ds_write_b64 v239, v[16:17] offset:2304
	v_mul_f32_e32 v20, s36, v20
	v_mul_f32_e32 v21, s36, v21
	v_mul_f32_e32 v22, s36, v22
	v_mul_f32_e32 v23, s36, v23
	v_cvt_pk_f16_f32 v20, v20, v21
	v_cvt_pk_f16_f32 v21, v22, v23
	ds_write_b64 v239, v[20:21] offset:2880
	v_mul_f32_e32 v24, s36, v24
	v_mul_f32_e32 v25, s36, v25
	v_mul_f32_e32 v26, s36, v26
	v_mul_f32_e32 v27, s36, v27
	v_cvt_pk_f16_f32 v24, v24, v25
	v_cvt_pk_f16_f32 v25, v26, v27
	ds_write_b64 v239, v[24:25] offset:3456
	v_mul_f32_e32 v28, s36, v28
	v_mul_f32_e32 v29, s36, v29
	v_mul_f32_e32 v30, s36, v30
	v_mul_f32_e32 v31, s36, v31
	v_cvt_pk_f16_f32 v28, v28, v29
	v_cvt_pk_f16_f32 v29, v30, v31
	ds_write_b64 v239, v[28:29] offset:4032
	s_waitcnt lgkmcnt(0)
	ds_read_b128 v[128:131], v240 offset:0
	ds_read_b128 v[132:135], v240 offset:32
	ds_read_b128 v[136:139], v240 offset:64
	ds_read_b128 v[140:143], v240 offset:96
	s_waitcnt lgkmcnt(0)
	v_mul_f32_e32 v32, s36, v32
	v_mul_f32_e32 v33, s36, v33
	v_mul_f32_e32 v34, s36, v34
	v_mul_f32_e32 v35, s36, v35
	v_cvt_pk_f16_f32 v32, v32, v33
	v_cvt_pk_f16_f32 v33, v34, v35
	ds_write_b64 v239, v[32:33] offset:0
	v_mul_f32_e32 v36, s36, v36
	v_mul_f32_e32 v37, s36, v37
	v_mul_f32_e32 v38, s36, v38
	v_mul_f32_e32 v39, s36, v39
	v_cvt_pk_f16_f32 v36, v36, v37
	v_cvt_pk_f16_f32 v37, v38, v39
	ds_write_b64 v239, v[36:37] offset:576
	v_mul_f32_e32 v40, s36, v40
	v_mul_f32_e32 v41, s36, v41
	v_mul_f32_e32 v42, s36, v42
	v_mul_f32_e32 v43, s36, v43
	v_cvt_pk_f16_f32 v40, v40, v41
	v_cvt_pk_f16_f32 v41, v42, v43
	ds_write_b64 v239, v[40:41] offset:1152
	v_mul_f32_e32 v44, s36, v44
	v_mul_f32_e32 v45, s36, v45
	v_mul_f32_e32 v46, s36, v46
	v_mul_f32_e32 v47, s36, v47
	v_cvt_pk_f16_f32 v44, v44, v45
	v_cvt_pk_f16_f32 v45, v46, v47
	ds_write_b64 v239, v[44:45] offset:1728
	v_mul_f32_e32 v48, s36, v48
	v_mul_f32_e32 v49, s36, v49
	v_mul_f32_e32 v50, s36, v50
	v_mul_f32_e32 v51, s36, v51
	v_cvt_pk_f16_f32 v48, v48, v49
	v_cvt_pk_f16_f32 v49, v50, v51
	ds_write_b64 v239, v[48:49] offset:2304
	v_mul_f32_e32 v52, s36, v52
	v_mul_f32_e32 v53, s36, v53
	v_mul_f32_e32 v54, s36, v54
	v_mul_f32_e32 v55, s36, v55
	v_cvt_pk_f16_f32 v52, v52, v53
	v_cvt_pk_f16_f32 v53, v54, v55
	ds_write_b64 v239, v[52:53] offset:2880
	v_mul_f32_e32 v56, s36, v56
	v_mul_f32_e32 v57, s36, v57
	v_mul_f32_e32 v58, s36, v58
	v_mul_f32_e32 v59, s36, v59
	v_cvt_pk_f16_f32 v56, v56, v57
	v_cvt_pk_f16_f32 v57, v58, v59
	ds_write_b64 v239, v[56:57] offset:3456
	v_mul_f32_e32 v60, s36, v60
	v_mul_f32_e32 v61, s36, v61
	v_mul_f32_e32 v62, s36, v62
	v_mul_f32_e32 v63, s36, v63
	v_cvt_pk_f16_f32 v60, v60, v61
	v_cvt_pk_f16_f32 v61, v62, v63
	ds_write_b64 v239, v[60:61] offset:4032
	s_waitcnt lgkmcnt(0)
	ds_read_b128 v[144:147], v240 offset:0
	ds_read_b128 v[148:151], v240 offset:32
	ds_read_b128 v[152:155], v240 offset:64
	ds_read_b128 v[156:159], v240 offset:96
	s_waitcnt lgkmcnt(0)
	s_barrier
	ds_read_b128 v[176:179], v225 offset:0
	ds_read_b128 v[180:183], v225 offset:32
	ds_read_b128 v[184:187], v225 offset:64
	ds_read_b128 v[188:191], v225 offset:96
	ds_read_b128 v[192:195], v225 offset:4608
	ds_read_b128 v[196:199], v225 offset:4640
	ds_read_b128 v[200:203], v225 offset:4672
	ds_read_b128 v[204:207], v225 offset:4704
	s_waitcnt lgkmcnt(0)
	v_cmp_ne_u32_e64 s[20:21], 0, v224
	v_mfma_f32_32x32x16_f16 v[64:79], v[176:179], v[128:131], 0
	v_mfma_f32_32x32x16_f16 v[64:79], v[180:183], v[132:135], v[64:79]
	v_mfma_f32_32x32x16_f16 v[64:79], v[184:187], v[136:139], v[64:79]
	v_mfma_f32_32x32x16_f16 v[64:79], v[188:191], v[140:143], v[64:79]
	v_mfma_f32_32x32x16_f16 v[80:95], v[192:195], v[128:131], 0
	v_mfma_f32_32x32x16_f16 v[80:95], v[196:199], v[132:135], v[80:95]
	v_mfma_f32_32x32x16_f16 v[80:95], v[200:203], v[136:139], v[80:95]
	v_mfma_f32_32x32x16_f16 v[80:95], v[204:207], v[140:143], v[80:95]
	s_nop 15
	s_nop 3
	s_cmp_eq_u64 s[20:21], -1
	s_cbranch_scc1 .Lpro_nomask_A
	v_lshrrev_b32_e64 v235, v234, s20
	v_bfe_u32 v236, v235, 0, 1
	v_cvt_f32_u32_e32 v236, v236
	v_sub_f32_e32 v236, 1.0, v236
	v_fmac_f32_e32 v64, s35, v236
	v_bfe_u32 v236, v235, 1, 1
	v_cvt_f32_u32_e32 v236, v236
	v_sub_f32_e32 v236, 1.0, v236
	v_fmac_f32_e32 v65, s35, v236
	v_bfe_u32 v236, v235, 2, 1
	v_cvt_f32_u32_e32 v236, v236
	v_sub_f32_e32 v236, 1.0, v236
	v_fmac_f32_e32 v66, s35, v236
	v_bfe_u32 v236, v235, 3, 1
	v_cvt_f32_u32_e32 v236, v236
	v_sub_f32_e32 v236, 1.0, v236
	v_fmac_f32_e32 v67, s35, v236
	v_bfe_u32 v236, v235, 8, 1
	v_cvt_f32_u32_e32 v236, v236
	v_sub_f32_e32 v236, 1.0, v236
	v_fmac_f32_e32 v68, s35, v236
	v_bfe_u32 v236, v235, 9, 1
	v_cvt_f32_u32_e32 v236, v236
	v_sub_f32_e32 v236, 1.0, v236
	v_fmac_f32_e32 v69, s35, v236
	v_bfe_u32 v236, v235, 10, 1
	v_cvt_f32_u32_e32 v236, v236
	v_sub_f32_e32 v236, 1.0, v236
	v_fmac_f32_e32 v70, s35, v236
	v_bfe_u32 v236, v235, 11, 1
	v_cvt_f32_u32_e32 v236, v236
	v_sub_f32_e32 v236, 1.0, v236
	v_fmac_f32_e32 v71, s35, v236
	v_bfe_u32 v236, v235, 16, 1
	v_cvt_f32_u32_e32 v236, v236
	v_sub_f32_e32 v236, 1.0, v236
	v_fmac_f32_e32 v72, s35, v236
	v_bfe_u32 v236, v235, 17, 1
	v_cvt_f32_u32_e32 v236, v236
	v_sub_f32_e32 v236, 1.0, v236
	v_fmac_f32_e32 v73, s35, v236
	v_bfe_u32 v236, v235, 18, 1
	v_cvt_f32_u32_e32 v236, v236
	v_sub_f32_e32 v236, 1.0, v236
	v_fmac_f32_e32 v74, s35, v236
	v_bfe_u32 v236, v235, 19, 1
	v_cvt_f32_u32_e32 v236, v236
	v_sub_f32_e32 v236, 1.0, v236
	v_fmac_f32_e32 v75, s35, v236
	v_bfe_u32 v236, v235, 24, 1
	v_cvt_f32_u32_e32 v236, v236
	v_sub_f32_e32 v236, 1.0, v236
	v_fmac_f32_e32 v76, s35, v236
	v_bfe_u32 v236, v235, 25, 1
	v_cvt_f32_u32_e32 v236, v236
	v_sub_f32_e32 v236, 1.0, v236
	v_fmac_f32_e32 v77, s35, v236
	v_bfe_u32 v236, v235, 26, 1
	v_cvt_f32_u32_e32 v236, v236
	v_sub_f32_e32 v236, 1.0, v236
	v_fmac_f32_e32 v78, s35, v236
	v_bfe_u32 v236, v235, 27, 1
	v_cvt_f32_u32_e32 v236, v236
	v_sub_f32_e32 v236, 1.0, v236
	v_fmac_f32_e32 v79, s35, v236
	v_lshrrev_b32_e64 v235, v234, s21
	v_bfe_u32 v236, v235, 0, 1
	v_cvt_f32_u32_e32 v236, v236
	v_sub_f32_e32 v236, 1.0, v236
	v_fmac_f32_e32 v80, s35, v236
	v_bfe_u32 v236, v235, 1, 1
	v_cvt_f32_u32_e32 v236, v236
	v_sub_f32_e32 v236, 1.0, v236
	v_fmac_f32_e32 v81, s35, v236
	v_bfe_u32 v236, v235, 2, 1
	v_cvt_f32_u32_e32 v236, v236
	v_sub_f32_e32 v236, 1.0, v236
	v_fmac_f32_e32 v82, s35, v236
	v_bfe_u32 v236, v235, 3, 1
	v_cvt_f32_u32_e32 v236, v236
	v_sub_f32_e32 v236, 1.0, v236
	v_fmac_f32_e32 v83, s35, v236
	v_bfe_u32 v236, v235, 8, 1
	v_cvt_f32_u32_e32 v236, v236
	v_sub_f32_e32 v236, 1.0, v236
	v_fmac_f32_e32 v84, s35, v236
	v_bfe_u32 v236, v235, 9, 1
	v_cvt_f32_u32_e32 v236, v236
	v_sub_f32_e32 v236, 1.0, v236
	v_fmac_f32_e32 v85, s35, v236
	v_bfe_u32 v236, v235, 10, 1
	v_cvt_f32_u32_e32 v236, v236
	v_sub_f32_e32 v236, 1.0, v236
	v_fmac_f32_e32 v86, s35, v236
	v_bfe_u32 v236, v235, 11, 1
	v_cvt_f32_u32_e32 v236, v236
	v_sub_f32_e32 v236, 1.0, v236
	v_fmac_f32_e32 v87, s35, v236
	v_bfe_u32 v236, v235, 16, 1
	v_cvt_f32_u32_e32 v236, v236
	v_sub_f32_e32 v236, 1.0, v236
	v_fmac_f32_e32 v88, s35, v236
	v_bfe_u32 v236, v235, 17, 1
	v_cvt_f32_u32_e32 v236, v236
	v_sub_f32_e32 v236, 1.0, v236
	v_fmac_f32_e32 v89, s35, v236
	v_bfe_u32 v236, v235, 18, 1
	v_cvt_f32_u32_e32 v236, v236
	v_sub_f32_e32 v236, 1.0, v236
	v_fmac_f32_e32 v90, s35, v236
	v_bfe_u32 v236, v235, 19, 1
	v_cvt_f32_u32_e32 v236, v236
	v_sub_f32_e32 v236, 1.0, v236
	v_fmac_f32_e32 v91, s35, v236
	v_bfe_u32 v236, v235, 24, 1
	v_cvt_f32_u32_e32 v236, v236
	v_sub_f32_e32 v236, 1.0, v236
	v_fmac_f32_e32 v92, s35, v236
	v_bfe_u32 v236, v235, 25, 1
	v_cvt_f32_u32_e32 v236, v236
	v_sub_f32_e32 v236, 1.0, v236
	v_fmac_f32_e32 v93, s35, v236
	v_bfe_u32 v236, v235, 26, 1
	v_cvt_f32_u32_e32 v236, v236
	v_sub_f32_e32 v236, 1.0, v236
	v_fmac_f32_e32 v94, s35, v236
	v_bfe_u32 v236, v235, 27, 1
	v_cvt_f32_u32_e32 v236, v236
	v_sub_f32_e32 v236, 1.0, v236
	v_fmac_f32_e32 v95, s35, v236
.Lpro_nomask_A:
	v_max3_f32 v235, v64, v65, v66
	v_max3_f32 v235, v235, v67, v68
	v_max3_f32 v235, v235, v69, v70
	v_max3_f32 v235, v235, v71, v72
	v_max3_f32 v235, v235, v73, v74
	v_max3_f32 v235, v235, v75, v76
	v_max3_f32 v235, v235, v77, v78
	v_max3_f32 v235, v235, v79, v80
	v_max3_f32 v235, v235, v81, v82
	v_max3_f32 v235, v235, v83, v84
	v_max3_f32 v235, v235, v85, v86
	v_max3_f32 v235, v235, v87, v88
	v_max3_f32 v235, v235, v89, v90
	v_max3_f32 v235, v235, v91, v92
	v_max3_f32 v235, v235, v93, v94
	v_max_f32_e32 v235, v235, v95
	v_mov_b32_e32 v236, v235
	s_nop 1
	v_permlane32_swap_b32_e32 v235, v236
	v_max_f32_e32 v235, v235, v236
	v_sub_f32_e32 v96, 0, v235
	v_sub_f32_e32 v97, 0, v235
	v_sub_f32_e32 v98, 0, v235
	v_sub_f32_e32 v99, 0, v235
	v_sub_f32_e32 v100, 0, v235
	v_sub_f32_e32 v101, 0, v235
	v_sub_f32_e32 v102, 0, v235
	v_sub_f32_e32 v103, 0, v235
	v_sub_f32_e32 v104, 0, v235
	v_sub_f32_e32 v105, 0, v235
	v_sub_f32_e32 v106, 0, v235
	v_sub_f32_e32 v107, 0, v235
	v_sub_f32_e32 v108, 0, v235
	v_sub_f32_e32 v109, 0, v235
	v_sub_f32_e32 v110, 0, v235
	v_sub_f32_e32 v111, 0, v235
	v_sub_f32_e32 v64, v64, v235
	v_sub_f32_e32 v65, v65, v235
	v_sub_f32_e32 v66, v66, v235
	v_sub_f32_e32 v67, v67, v235
	v_sub_f32_e32 v68, v68, v235
	v_sub_f32_e32 v69, v69, v235
	v_sub_f32_e32 v70, v70, v235
	v_sub_f32_e32 v71, v71, v235
	v_sub_f32_e32 v72, v72, v235
	v_sub_f32_e32 v73, v73, v235
	v_sub_f32_e32 v74, v74, v235
	v_sub_f32_e32 v75, v75, v235
	v_sub_f32_e32 v76, v76, v235
	v_sub_f32_e32 v77, v77, v235
	v_sub_f32_e32 v78, v78, v235
	v_sub_f32_e32 v79, v79, v235
	v_mfma_f32_32x32x16_f16 v[160:175], v[176:179], v[144:147], 0
	v_mfma_f32_32x32x16_f16 v[160:175], v[180:183], v[148:151], v[160:175]
	v_mfma_f32_32x32x16_f16 v[160:175], v[184:187], v[152:155], v[160:175]
	v_mfma_f32_32x32x16_f16 v[160:175], v[188:191], v[156:159], v[160:175]
	v_mfma_f32_32x32x16_f16 v[80:95], v[192:195], v[144:147], 0
	v_mfma_f32_32x32x16_f16 v[80:95], v[196:199], v[148:151], v[80:95]
	v_mfma_f32_32x32x16_f16 v[80:95], v[200:203], v[152:155], v[80:95]
	v_mfma_f32_32x32x16_f16 v[80:95], v[204:207], v[156:159], v[80:95]
	s_nop 15
	s_nop 3
	s_cmp_eq_u64 s[20:21], -1
	s_cbranch_scc1 .Lpro_nomask_B
	v_lshrrev_b32_e64 v235, v234, s20
	v_bfe_u32 v236, v235, 0, 1
	v_cvt_f32_u32_e32 v236, v236
	v_sub_f32_e32 v236, 1.0, v236
	v_fmac_f32_e32 v160, s35, v236
	v_bfe_u32 v236, v235, 1, 1
	v_cvt_f32_u32_e32 v236, v236
	v_sub_f32_e32 v236, 1.0, v236
	v_fmac_f32_e32 v161, s35, v236
	v_bfe_u32 v236, v235, 2, 1
	v_cvt_f32_u32_e32 v236, v236
	v_sub_f32_e32 v236, 1.0, v236
	v_fmac_f32_e32 v162, s35, v236
	v_bfe_u32 v236, v235, 3, 1
	v_cvt_f32_u32_e32 v236, v236
	v_sub_f32_e32 v236, 1.0, v236
	v_fmac_f32_e32 v163, s35, v236
	v_bfe_u32 v236, v235, 8, 1
	v_cvt_f32_u32_e32 v236, v236
	v_sub_f32_e32 v236, 1.0, v236
	v_fmac_f32_e32 v164, s35, v236
	v_bfe_u32 v236, v235, 9, 1
	v_cvt_f32_u32_e32 v236, v236
	v_sub_f32_e32 v236, 1.0, v236
	v_fmac_f32_e32 v165, s35, v236
	v_bfe_u32 v236, v235, 10, 1
	v_cvt_f32_u32_e32 v236, v236
	v_sub_f32_e32 v236, 1.0, v236
	v_fmac_f32_e32 v166, s35, v236
	v_bfe_u32 v236, v235, 11, 1
	v_cvt_f32_u32_e32 v236, v236
	v_sub_f32_e32 v236, 1.0, v236
	v_fmac_f32_e32 v167, s35, v236
	v_bfe_u32 v236, v235, 16, 1
	v_cvt_f32_u32_e32 v236, v236
	v_sub_f32_e32 v236, 1.0, v236
	v_fmac_f32_e32 v168, s35, v236
	v_bfe_u32 v236, v235, 17, 1
	v_cvt_f32_u32_e32 v236, v236
	v_sub_f32_e32 v236, 1.0, v236
	v_fmac_f32_e32 v169, s35, v236
	v_bfe_u32 v236, v235, 18, 1
	v_cvt_f32_u32_e32 v236, v236
	v_sub_f32_e32 v236, 1.0, v236
	v_fmac_f32_e32 v170, s35, v236
	v_bfe_u32 v236, v235, 19, 1
	v_cvt_f32_u32_e32 v236, v236
	v_sub_f32_e32 v236, 1.0, v236
	v_fmac_f32_e32 v171, s35, v236
	v_bfe_u32 v236, v235, 24, 1
	v_cvt_f32_u32_e32 v236, v236
	v_sub_f32_e32 v236, 1.0, v236
	v_fmac_f32_e32 v172, s35, v236
	v_bfe_u32 v236, v235, 25, 1
	v_cvt_f32_u32_e32 v236, v236
	v_sub_f32_e32 v236, 1.0, v236
	v_fmac_f32_e32 v173, s35, v236
	v_bfe_u32 v236, v235, 26, 1
	v_cvt_f32_u32_e32 v236, v236
	v_sub_f32_e32 v236, 1.0, v236
	v_fmac_f32_e32 v174, s35, v236
	v_bfe_u32 v236, v235, 27, 1
	v_cvt_f32_u32_e32 v236, v236
	v_sub_f32_e32 v236, 1.0, v236
	v_fmac_f32_e32 v175, s35, v236
	v_lshrrev_b32_e64 v235, v234, s21
	v_bfe_u32 v236, v235, 0, 1
	v_cvt_f32_u32_e32 v236, v236
	v_sub_f32_e32 v236, 1.0, v236
	v_fmac_f32_e32 v80, s35, v236
	v_bfe_u32 v236, v235, 1, 1
	v_cvt_f32_u32_e32 v236, v236
	v_sub_f32_e32 v236, 1.0, v236
	v_fmac_f32_e32 v81, s35, v236
	v_bfe_u32 v236, v235, 2, 1
	v_cvt_f32_u32_e32 v236, v236
	v_sub_f32_e32 v236, 1.0, v236
	v_fmac_f32_e32 v82, s35, v236
	v_bfe_u32 v236, v235, 3, 1
	v_cvt_f32_u32_e32 v236, v236
	v_sub_f32_e32 v236, 1.0, v236
	v_fmac_f32_e32 v83, s35, v236
	v_bfe_u32 v236, v235, 8, 1
	v_cvt_f32_u32_e32 v236, v236
	v_sub_f32_e32 v236, 1.0, v236
	v_fmac_f32_e32 v84, s35, v236
	v_bfe_u32 v236, v235, 9, 1
	v_cvt_f32_u32_e32 v236, v236
	v_sub_f32_e32 v236, 1.0, v236
	v_fmac_f32_e32 v85, s35, v236
	v_bfe_u32 v236, v235, 10, 1
	v_cvt_f32_u32_e32 v236, v236
	v_sub_f32_e32 v236, 1.0, v236
	v_fmac_f32_e32 v86, s35, v236
	v_bfe_u32 v236, v235, 11, 1
	v_cvt_f32_u32_e32 v236, v236
	v_sub_f32_e32 v236, 1.0, v236
	v_fmac_f32_e32 v87, s35, v236
	v_bfe_u32 v236, v235, 16, 1
	v_cvt_f32_u32_e32 v236, v236
	v_sub_f32_e32 v236, 1.0, v236
	v_fmac_f32_e32 v88, s35, v236
	v_bfe_u32 v236, v235, 17, 1
	v_cvt_f32_u32_e32 v236, v236
	v_sub_f32_e32 v236, 1.0, v236
	v_fmac_f32_e32 v89, s35, v236
	v_bfe_u32 v236, v235, 18, 1
	v_cvt_f32_u32_e32 v236, v236
	v_sub_f32_e32 v236, 1.0, v236
	v_fmac_f32_e32 v90, s35, v236
	v_bfe_u32 v236, v235, 19, 1
	v_cvt_f32_u32_e32 v236, v236
	v_sub_f32_e32 v236, 1.0, v236
	v_fmac_f32_e32 v91, s35, v236
	v_bfe_u32 v236, v235, 24, 1
	v_cvt_f32_u32_e32 v236, v236
	v_sub_f32_e32 v236, 1.0, v236
	v_fmac_f32_e32 v92, s35, v236
	v_bfe_u32 v236, v235, 25, 1
	v_cvt_f32_u32_e32 v236, v236
	v_sub_f32_e32 v236, 1.0, v236
	v_fmac_f32_e32 v93, s35, v236
	v_bfe_u32 v236, v235, 26, 1
	v_cvt_f32_u32_e32 v236, v236
	v_sub_f32_e32 v236, 1.0, v236
	v_fmac_f32_e32 v94, s35, v236
	v_bfe_u32 v236, v235, 27, 1
	v_cvt_f32_u32_e32 v236, v236
	v_sub_f32_e32 v236, 1.0, v236
	v_fmac_f32_e32 v95, s35, v236
.Lpro_nomask_B:
	v_max3_f32 v235, v160, v161, v162
	v_max3_f32 v235, v235, v163, v164
	v_max3_f32 v235, v235, v165, v166
	v_max3_f32 v235, v235, v167, v168
	v_max3_f32 v235, v235, v169, v170
	v_max3_f32 v235, v235, v171, v172
	v_max3_f32 v235, v235, v173, v174
	v_max3_f32 v235, v235, v175, v80
	v_max3_f32 v235, v235, v81, v82
	v_max3_f32 v235, v235, v83, v84
	v_max3_f32 v235, v235, v85, v86
	v_max3_f32 v235, v235, v87, v88
	v_max3_f32 v235, v235, v89, v90
	v_max3_f32 v235, v235, v91, v92
	v_max3_f32 v235, v235, v93, v94
	v_max_f32_e32 v235, v235, v95
	v_mov_b32_e32 v236, v235
	s_nop 1
	v_permlane32_swap_b32_e32 v235, v236
	v_max_f32_e32 v235, v235, v236
	v_sub_f32_e32 v112, 0, v235
	v_sub_f32_e32 v113, 0, v235
	v_sub_f32_e32 v114, 0, v235
	v_sub_f32_e32 v115, 0, v235
	v_sub_f32_e32 v116, 0, v235
	v_sub_f32_e32 v117, 0, v235
	v_sub_f32_e32 v118, 0, v235
	v_sub_f32_e32 v119, 0, v235
	v_sub_f32_e32 v120, 0, v235
	v_sub_f32_e32 v121, 0, v235
	v_sub_f32_e32 v122, 0, v235
	v_sub_f32_e32 v123, 0, v235
	v_sub_f32_e32 v124, 0, v235
	v_sub_f32_e32 v125, 0, v235
	v_sub_f32_e32 v126, 0, v235
	v_sub_f32_e32 v127, 0, v235
	v_mov_b32_e32 v0, 0
	v_mov_b32_e32 v1, 0
	v_mov_b32_e32 v2, 0
	v_mov_b32_e32 v3, 0
	v_mov_b32_e32 v4, 0
	v_mov_b32_e32 v5, 0
	v_mov_b32_e32 v6, 0
	v_mov_b32_e32 v7, 0
	v_mov_b32_e32 v8, 0
	v_mov_b32_e32 v9, 0
	v_mov_b32_e32 v10, 0
	v_mov_b32_e32 v11, 0
	v_mov_b32_e32 v12, 0
	v_mov_b32_e32 v13, 0
	v_mov_b32_e32 v14, 0
	v_mov_b32_e32 v15, 0
	v_mov_b32_e32 v16, 0
	v_mov_b32_e32 v17, 0
	v_mov_b32_e32 v18, 0
	v_mov_b32_e32 v19, 0
	v_mov_b32_e32 v20, 0
	v_mov_b32_e32 v21, 0
	v_mov_b32_e32 v22, 0
	v_mov_b32_e32 v23, 0
	v_mov_b32_e32 v24, 0
	v_mov_b32_e32 v25, 0
	v_mov_b32_e32 v26, 0
	v_mov_b32_e32 v27, 0
	v_mov_b32_e32 v28, 0
	v_mov_b32_e32 v29, 0
	v_mov_b32_e32 v30, 0
	v_mov_b32_e32 v31, 0
	v_mov_b32_e32 v32, 0
	v_mov_b32_e32 v33, 0
	v_mov_b32_e32 v34, 0
	v_mov_b32_e32 v35, 0
	v_mov_b32_e32 v36, 0
	v_mov_b32_e32 v37, 0
	v_mov_b32_e32 v38, 0
	v_mov_b32_e32 v39, 0
	v_mov_b32_e32 v40, 0
	v_mov_b32_e32 v41, 0
	v_mov_b32_e32 v42, 0
	v_mov_b32_e32 v43, 0
	v_mov_b32_e32 v44, 0
	v_mov_b32_e32 v45, 0
	v_mov_b32_e32 v46, 0
	v_mov_b32_e32 v47, 0
	v_mov_b32_e32 v48, 0
	v_mov_b32_e32 v49, 0
	v_mov_b32_e32 v50, 0
	v_mov_b32_e32 v51, 0
	v_mov_b32_e32 v52, 0
	v_mov_b32_e32 v53, 0
	v_mov_b32_e32 v54, 0
	v_mov_b32_e32 v55, 0
	v_mov_b32_e32 v56, 0
	v_mov_b32_e32 v57, 0
	v_mov_b32_e32 v58, 0
	v_mov_b32_e32 v59, 0
	v_mov_b32_e32 v60, 0
	v_mov_b32_e32 v61, 0
	v_mov_b32_e32 v62, 0
	v_mov_b32_e32 v63, 0
	v_mov_b32_e32 v168, 0
	v_mov_b32_e32 v169, 0
	v_mov_b32_e32 v170, 0
	v_mov_b32_e32 v171, 0
	v_mov_b32_e32 v172, 0
	v_mov_b32_e32 v173, 0
	v_mov_b32_e32 v174, 0
	v_mov_b32_e32 v175, 0
	v_mov_b32_e32 v232, 0
	v_mov_b32_e32 v233, 0
.Lbody:
	s_waitcnt vmcnt(8)
	v_cmp_ne_u32_e64 s[20:21], 0, v224
	s_add_u32 s31, s23, 1
	s_and_b32 s31, s31, 31
	s_lshl_b32 s31, s31, 8
	s_add_u32 s26, s31, s22
	s_add_u32 s31, s23, 3
	s_and_b32 s31, s31, 31
	s_mul_i32 s31, s31, 0xc0000
	s_add_u32 s24, s31, s18
	s_add_u32 s25, s31, s19
	s_cmp_eq_u64 s[20:21], -1
	s_cselect_b32 s34, s37, s38
	s_waitcnt lgkmcnt(4)
	v_mfma_f32_32x32x16_f16 v[80:95], v[176:179], v[144:147], v[112:127]
	ds_read_b128 v[176:179], v225 offset:4608
	v_exp_f32_e32 v64, v64
	v_exp_f32_e32 v65, v65
	buffer_load_dword v224, v230, s[8:11], s26 offen
	v_cvt_pk_f16_f32 v208, v208, v209
	v_cvt_pk_f16_f32 v209, v210, v211
	v_mfma_f32_32x32x16_f16 v[80:95], v[180:183], v[148:151], v[80:95]
	ds_read_b128 v[180:183], v225 offset:4640
	v_exp_f32_e32 v66, v66
	v_exp_f32_e32 v67, v67
	v_cvt_pk_f16_f32 v212, v212, v213
	v_cvt_pk_f16_f32 v160, v64, v65
	v_add_f32_e32 v64, v64, v65
	v_cvt_pk_f16_f32 v213, v214, v215
	v_mfma_f32_32x32x16_f16 v[80:95], v[184:187], v[152:155], v[80:95]
	ds_write_b64 v227, v[208:209] offset:18432
	ds_write_b64 v227, v[212:213] offset:23040
	ds_read_b128 v[184:187], v225 offset:4672
	v_exp_f32_e32 v68, v68
	v_exp_f32_e32 v69, v69
	v_cvt_pk_f16_f32 v161, v66, v67
	v_add_f32_e32 v66, v66, v67
	v_mfma_f32_32x32x16_f16 v[80:95], v[188:191], v[156:159], v[80:95]
	ds_read_b128 v[188:191], v225 offset:4704
	v_exp_f32_e32 v70, v70
	v_exp_f32_e32 v71, v71
	v_cvt_pk_f16_f32 v162, v68, v69
	v_add_f32_e32 v68, v68, v69
	v_add_f32_e32 v231, v64, v66
	s_waitcnt lgkmcnt(6)
	v_mfma_f32_32x32x16_f16 v[32:47], v[192:195], v[168:171], v[32:47]
	ds_read_b128 v[192:195], v226 offset:0
	v_exp_f32_e32 v72, v72
	v_exp_f32_e32 v73, v73
	v_cvt_pk_f16_f32 v163, v70, v71
	v_add_f32_e32 v70, v70, v71
	v_add_f32_e32 v231, v231, v68
	v_mfma_f32_32x32x16_f16 v[48:63], v[196:199], v[168:171], v[48:63]
	ds_read_b128 v[196:199], v226 offset:4608
	v_exp_f32_e32 v74, v74
	v_exp_f32_e32 v75, v75
	v_cvt_pk_f16_f32 v164, v72, v73
	v_add_f32_e32 v72, v72, v73
	v_add_f32_e32 v231, v231, v70
	v_mfma_f32_32x32x16_f16 v[32:47], v[200:203], v[172:175], v[32:47]
	ds_read_b128 v[200:203], v226 offset:32
	v_exp_f32_e32 v76, v76
	v_exp_f32_e32 v77, v77
	v_cvt_pk_f16_f32 v165, v74, v75
	v_add_f32_e32 v74, v74, v75
	v_add_f32_e32 v231, v231, v72
	v_mfma_f32_32x32x16_f16 v[48:63], v[204:207], v[172:175], v[48:63]
	ds_read_b128 v[204:207], v226 offset:4640
	v_exp_f32_e32 v78, v78
	v_exp_f32_e32 v79, v79
	v_cvt_pk_f16_f32 v166, v76, v77
	v_add_f32_e32 v76, v76, v77
	v_add_f32_e32 v231, v231, v74
	v_cvt_pk_f16_f32 v167, v78, v79
	v_add_f32_e32 v78, v78, v79
	v_add_f32_e32 v231, v231, v76
	v_add_f32_e32 v231, v231, v78
	v_cmp_nge_f32_e32 vcc, s34, v231
	s_cbranch_vccnz .Lovf_a00
.Lovfret_a00:
	v_add_f32_e32 v232, v232, v231
	s_waitcnt lgkmcnt(4)
	v_mfma_f32_32x32x16_f16 v[64:79], v[176:179], v[128:131], v[96:111]
	v_exp_f32_e32 v80, v80
	v_exp_f32_e32 v81, v81
	v_mfma_f32_32x32x16_f16 v[64:79], v[180:183], v[132:135], v[64:79]
	v_exp_f32_e32 v82, v82
	v_exp_f32_e32 v83, v83
	buffer_load_dwordx4 v[208:211], v229, s[4:7], s24 offen
	v_cvt_pk_f16_f32 v168, v80, v81
	v_add_f32_e32 v80, v80, v81
	v_mfma_f32_32x32x16_f16 v[64:79], v[184:187], v[136:139], v[64:79]
	v_exp_f32_e32 v84, v84
	v_exp_f32_e32 v85, v85
	s_add_u32 s31, s24, 0x60000
	v_cvt_pk_f16_f32 v169, v82, v83
	v_add_f32_e32 v82, v82, v83
	buffer_load_dwordx4 v[212:215], v229, s[4:7], s31 offen
	v_mfma_f32_32x32x16_f16 v[64:79], v[188:191], v[140:143], v[64:79]
	v_exp_f32_e32 v86, v86
	v_exp_f32_e32 v87, v87
	v_cvt_pk_f16_f32 v170, v84, v85
	v_add_f32_e32 v84, v84, v85
	v_add_f32_e32 v231, v80, v82
	s_waitcnt lgkmcnt(0)
	v_mfma_f32_32x32x16_f16 v[0:15], v[192:195], v[160:163], v[0:15]
	v_exp_f32_e32 v88, v88
	v_exp_f32_e32 v89, v89
	v_cvt_pk_f16_f32 v171, v86, v87
	v_add_f32_e32 v86, v86, v87
	v_add_f32_e32 v231, v231, v84
	v_mfma_f32_32x32x16_f16 v[16:31], v[196:199], v[160:163], v[16:31]
	v_exp_f32_e32 v90, v90
	v_exp_f32_e32 v91, v91
	v_cvt_pk_f16_f32 v172, v88, v89
	v_add_f32_e32 v88, v88, v89
	v_add_f32_e32 v231, v231, v86
	v_mfma_f32_32x32x16_f16 v[0:15], v[200:203], v[164:167], v[0:15]
	v_exp_f32_e32 v92, v92
	v_exp_f32_e32 v93, v93
	v_cvt_pk_f16_f32 v173, v90, v91
	v_add_f32_e32 v90, v90, v91
	v_add_f32_e32 v231, v231, v88
	v_mfma_f32_32x32x16_f16 v[16:31], v[204:207], v[164:167], v[16:31]
	v_exp_f32_e32 v94, v94
	v_exp_f32_e32 v95, v95
	v_cvt_pk_f16_f32 v174, v92, v93
	v_add_f32_e32 v92, v92, v93
	v_add_f32_e32 v231, v231, v90
	v_cvt_pk_f16_f32 v175, v94, v95
	v_add_f32_e32 v94, v94, v95
	v_add_f32_e32 v231, v231, v92
	v_add_f32_e32 v231, v231, v94
	v_cmp_nge_f32_e32 vcc, s34, v231
	s_cbranch_vccnz .Lovf_b00
.Lovfret_b00:
	v_add_f32_e32 v233, v233, v231
	s_waitcnt lgkmcnt(4)
	v_mfma_f32_32x32x16_f16 v[80:95], v[176:179], v[144:147], v[112:127]
	ds_read_b128 v[176:179], v225 offset:9216
	v_exp_f32_e32 v64, v64
	v_exp_f32_e32 v65, v65
	s_waitcnt vmcnt(3)
	v_cvt_pk_f16_f32 v216, v216, v217
	v_cvt_pk_f16_f32 v217, v218, v219
	v_mfma_f32_32x32x16_f16 v[80:95], v[180:183], v[148:151], v[80:95]
	ds_read_b128 v[180:183], v225 offset:9248
	v_exp_f32_e32 v66, v66
	v_exp_f32_e32 v67, v67
	v_cvt_pk_f16_f32 v218, v220, v221
	v_cvt_pk_f16_f32 v160, v64, v65
	v_add_f32_e32 v64, v64, v65
	v_cvt_pk_f16_f32 v219, v222, v223
	v_mfma_f32_32x32x16_f16 v[80:95], v[184:187], v[152:155], v[80:95]
	ds_write_b128 v228, v[216:219] offset:18432
	ds_read_b128 v[184:187], v225 offset:9280
	v_exp_f32_e32 v68, v68
	v_exp_f32_e32 v69, v69
	v_cvt_pk_f16_f32 v161, v66, v67
	v_add_f32_e32 v66, v66, v67
	v_mfma_f32_32x32x16_f16 v[80:95], v[188:191], v[156:159], v[80:95]
	ds_read_b128 v[188:191], v225 offset:9312
	v_exp_f32_e32 v70, v70
	v_exp_f32_e32 v71, v71
	v_cvt_pk_f16_f32 v162, v68, v69
	v_add_f32_e32 v68, v68, v69
	v_add_f32_e32 v231, v64, v66
	s_waitcnt lgkmcnt(5)
	v_mfma_f32_32x32x16_f16 v[32:47], v[192:195], v[168:171], v[32:47]
	ds_read_b128 v[192:195], v226 offset:64
	v_exp_f32_e32 v72, v72
	v_exp_f32_e32 v73, v73
	v_cvt_pk_f16_f32 v163, v70, v71
	v_add_f32_e32 v70, v70, v71
	v_add_f32_e32 v231, v231, v68
	v_mfma_f32_32x32x16_f16 v[48:63], v[196:199], v[168:171], v[48:63]
	ds_read_b128 v[196:199], v226 offset:4672
	v_exp_f32_e32 v74, v74
	v_exp_f32_e32 v75, v75
	v_cvt_pk_f16_f32 v164, v72, v73
	v_add_f32_e32 v72, v72, v73
	v_add_f32_e32 v231, v231, v70
	v_mfma_f32_32x32x16_f16 v[32:47], v[200:203], v[172:175], v[32:47]
	ds_read_b128 v[200:203], v226 offset:96
	v_exp_f32_e32 v76, v76
	v_exp_f32_e32 v77, v77
	v_cvt_pk_f16_f32 v165, v74, v75
	v_add_f32_e32 v74, v74, v75
	v_add_f32_e32 v231, v231, v72
	v_mfma_f32_32x32x16_f16 v[48:63], v[204:207], v[172:175], v[48:63]
	ds_read_b128 v[204:207], v226 offset:4704
	v_exp_f32_e32 v78, v78
	v_exp_f32_e32 v79, v79
	v_cvt_pk_f16_f32 v166, v76, v77
	v_add_f32_e32 v76, v76, v77
	v_add_f32_e32 v231, v231, v74
	v_cvt_pk_f16_f32 v167, v78, v79
	v_add_f32_e32 v78, v78, v79
	v_add_f32_e32 v231, v231, v76
	v_add_f32_e32 v231, v231, v78
	v_cmp_nge_f32_e32 vcc, s34, v231
	s_cbranch_vccnz .Lovf_a01
.Lovfret_a01:
	v_add_f32_e32 v232, v232, v231
	s_waitcnt lgkmcnt(4)
	v_mfma_f32_32x32x16_f16 v[64:79], v[176:179], v[128:131], v[96:111]
	v_exp_f32_e32 v80, v80
	v_exp_f32_e32 v81, v81
	buffer_load_dword v216, v230, s[4:7], s25 offen
	v_mfma_f32_32x32x16_f16 v[64:79], v[180:183], v[132:135], v[64:79]
	v_exp_f32_e32 v82, v82
	v_exp_f32_e32 v83, v83
	s_add_u32 s31, s25, 0x3000
	v_cvt_pk_f16_f32 v168, v80, v81
	v_add_f32_e32 v80, v80, v81
	buffer_load_dword v217, v230, s[4:7], s31 offen
	v_mfma_f32_32x32x16_f16 v[64:79], v[184:187], v[136:139], v[64:79]
	v_exp_f32_e32 v84, v84
	v_exp_f32_e32 v85, v85
	s_add_u32 s31, s25, 0x6000
	v_cvt_pk_f16_f32 v169, v82, v83
	v_add_f32_e32 v82, v82, v83
	buffer_load_dword v218, v230, s[4:7], s31 offen
	v_mfma_f32_32x32x16_f16 v[64:79], v[188:191], v[140:143], v[64:79]
	v_exp_f32_e32 v86, v86
	v_exp_f32_e32 v87, v87
	s_add_u32 s31, s25, 0x9000
	v_cvt_pk_f16_f32 v170, v84, v85
	v_add_f32_e32 v84, v84, v85
	buffer_load_dword v219, v230, s[4:7], s31 offen
	v_add_f32_e32 v231, v80, v82
	s_waitcnt lgkmcnt(0)
	v_mfma_f32_32x32x16_f16 v[0:15], v[192:195], v[160:163], v[0:15]
	v_exp_f32_e32 v88, v88
	v_exp_f32_e32 v89, v89
	s_add_u32 s31, s25, 0x18000
	v_cvt_pk_f16_f32 v171, v86, v87
	v_add_f32_e32 v86, v86, v87
	buffer_load_dword v220, v230, s[4:7], s31 offen
	v_add_f32_e32 v231, v231, v84
	v_mfma_f32_32x32x16_f16 v[16:31], v[196:199], v[160:163], v[16:31]
	v_exp_f32_e32 v90, v90
	v_exp_f32_e32 v91, v91
	s_add_u32 s31, s25, 0x1b000
	v_cvt_pk_f16_f32 v172, v88, v89
	v_add_f32_e32 v88, v88, v89
	buffer_load_dword v221, v230, s[4:7], s31 offen
	v_add_f32_e32 v231, v231, v86
	v_mfma_f32_32x32x16_f16 v[0:15], v[200:203], v[164:167], v[0:15]
	v_exp_f32_e32 v92, v92
	v_exp_f32_e32 v93, v93
	s_add_u32 s31, s25, 0x1e000
	v_cvt_pk_f16_f32 v173, v90, v91
	v_add_f32_e32 v90, v90, v91
	buffer_load_dword v222, v230, s[4:7], s31 offen
	v_add_f32_e32 v231, v231, v88
	v_mfma_f32_32x32x16_f16 v[16:31], v[204:207], v[164:167], v[16:31]
	v_exp_f32_e32 v94, v94
	v_exp_f32_e32 v95, v95
	s_add_u32 s31, s25, 0x21000
	v_cvt_pk_f16_f32 v174, v92, v93
	v_add_f32_e32 v92, v92, v93
	buffer_load_dword v223, v230, s[4:7], s31 offen
	v_add_f32_e32 v231, v231, v90
	v_cvt_pk_f16_f32 v175, v94, v95
	v_add_f32_e32 v94, v94, v95
	v_add_f32_e32 v231, v231, v92
	v_add_f32_e32 v231, v231, v94
	v_cmp_nge_f32_e32 vcc, s34, v231
	s_cbranch_vccnz .Lovf_b01
.Lovfret_b01:
	v_add_f32_e32 v233, v233, v231
	s_waitcnt lgkmcnt(6)
	s_barrier
	s_add_u32 s23, s23, 1
	s_waitcnt vmcnt(8)
	v_cmp_ne_u32_e64 s[20:21], 0, v224
	s_add_u32 s31, s23, 1
	s_and_b32 s31, s31, 31
	s_lshl_b32 s31, s31, 8
	s_add_u32 s26, s31, s22
	s_add_u32 s31, s23, 3
	s_and_b32 s31, s31, 31
	s_mul_i32 s31, s31, 0xc0000
	s_add_u32 s24, s31, s18
	s_add_u32 s25, s31, s19
	s_cmp_eq_u64 s[20:21], -1
	s_cselect_b32 s34, s37, s38
	s_waitcnt lgkmcnt(4)
	v_mfma_f32_32x32x16_f16 v[80:95], v[176:179], v[144:147], v[112:127]
	ds_read_b128 v[176:179], v225 offset:13824
	v_exp_f32_e32 v64, v64
	v_exp_f32_e32 v65, v65
	buffer_load_dword v224, v230, s[8:11], s26 offen
	v_cvt_pk_f16_f32 v208, v208, v209
	v_cvt_pk_f16_f32 v209, v210, v211
	v_mfma_f32_32x32x16_f16 v[80:95], v[180:183], v[148:151], v[80:95]
	ds_read_b128 v[180:183], v225 offset:13856
	v_exp_f32_e32 v66, v66
	v_exp_f32_e32 v67, v67
	v_cvt_pk_f16_f32 v212, v212, v213
	v_cvt_pk_f16_f32 v160, v64, v65
	v_add_f32_e32 v64, v64, v65
	v_cvt_pk_f16_f32 v213, v214, v215
	v_mfma_f32_32x32x16_f16 v[80:95], v[184:187], v[152:155], v[80:95]
	ds_write_b64 v227, v[208:209] offset:27648
	ds_write_b64 v227, v[212:213] offset:32256
	ds_read_b128 v[184:187], v225 offset:13888
	v_exp_f32_e32 v68, v68
	v_exp_f32_e32 v69, v69
	v_cvt_pk_f16_f32 v161, v66, v67
	v_add_f32_e32 v66, v66, v67
	v_mfma_f32_32x32x16_f16 v[80:95], v[188:191], v[156:159], v[80:95]
	ds_read_b128 v[188:191], v225 offset:13920
	v_exp_f32_e32 v70, v70
	v_exp_f32_e32 v71, v71
	v_cvt_pk_f16_f32 v162, v68, v69
	v_add_f32_e32 v68, v68, v69
	v_add_f32_e32 v231, v64, v66
	s_waitcnt lgkmcnt(6)
	v_mfma_f32_32x32x16_f16 v[32:47], v[192:195], v[168:171], v[32:47]
	ds_read_b128 v[192:195], v226 offset:9216
	v_exp_f32_e32 v72, v72
	v_exp_f32_e32 v73, v73
	v_cvt_pk_f16_f32 v163, v70, v71
	v_add_f32_e32 v70, v70, v71
	v_add_f32_e32 v231, v231, v68
	v_mfma_f32_32x32x16_f16 v[48:63], v[196:199], v[168:171], v[48:63]
	ds_read_b128 v[196:199], v226 offset:13824
	v_exp_f32_e32 v74, v74
	v_exp_f32_e32 v75, v75
	v_cvt_pk_f16_f32 v164, v72, v73
	v_add_f32_e32 v72, v72, v73
	v_add_f32_e32 v231, v231, v70
	v_mfma_f32_32x32x16_f16 v[32:47], v[200:203], v[172:175], v[32:47]
	ds_read_b128 v[200:203], v226 offset:9248
	v_exp_f32_e32 v76, v76
	v_exp_f32_e32 v77, v77
	v_cvt_pk_f16_f32 v165, v74, v75
	v_add_f32_e32 v74, v74, v75
	v_add_f32_e32 v231, v231, v72
	v_mfma_f32_32x32x16_f16 v[48:63], v[204:207], v[172:175], v[48:63]
	ds_read_b128 v[204:207], v226 offset:13856
	v_exp_f32_e32 v78, v78
	v_exp_f32_e32 v79, v79
	v_cvt_pk_f16_f32 v166, v76, v77
	v_add_f32_e32 v76, v76, v77
	v_add_f32_e32 v231, v231, v74
	v_cvt_pk_f16_f32 v167, v78, v79
	v_add_f32_e32 v78, v78, v79
	v_add_f32_e32 v231, v231, v76
	v_add_f32_e32 v231, v231, v78
	v_cmp_nge_f32_e32 vcc, s34, v231
	s_cbranch_vccnz .Lovf_a10

.Lovfret_b10:
	v_add_f32_e32 v233, v233, v231
	s_waitcnt lgkmcnt(4)
	v_mfma_f32_32x32x16_f16 v[80:95], v[176:179], v[144:147], v[112:127]
	ds_read_b128 v[176:179], v225 offset:18432
	v_exp_f32_e32 v64, v64
	v_exp_f32_e32 v65, v65
	s_waitcnt vmcnt(3)
	v_cvt_pk_f16_f32 v216, v216, v217
	v_cvt_pk_f16_f32 v217, v218, v219
	v_mfma_f32_32x32x16_f16 v[80:95], v[180:183], v[148:151], v[80:95]
	ds_read_b128 v[180:183], v225 offset:18464
	v_exp_f32_e32 v66, v66
	v_exp_f32_e32 v67, v67
	v_cvt_pk_f16_f32 v218, v220, v221
	v_cvt_pk_f16_f32 v160, v64, v65
	v_add_f32_e32 v64, v64, v65
	v_cvt_pk_f16_f32 v219, v222, v223
	v_mfma_f32_32x32x16_f16 v[80:95], v[184:187], v[152:155], v[80:95]
	ds_write_b128 v228, v[216:219] offset:27648
	ds_read_b128 v[184:187], v225 offset:18496
	v_exp_f32_e32 v68, v68
	v_exp_f32_e32 v69, v69
	v_cvt_pk_f16_f32 v161, v66, v67
	v_add_f32_e32 v66, v66, v67
	v_mfma_f32_32x32x16_f16 v[80:95], v[188:191], v[156:159], v[80:95]
	ds_read_b128 v[188:191], v225 offset:18528
	v_exp_f32_e32 v70, v70
	v_exp_f32_e32 v71, v71
	v_cvt_pk_f16_f32 v162, v68, v69
	v_add_f32_e32 v68, v68, v69
	v_add_f32_e32 v231, v64, v66
	s_waitcnt lgkmcnt(5)
	v_mfma_f32_32x32x16_f16 v[32:47], v[192:195], v[168:171], v[32:47]
	ds_read_b128 v[192:195], v226 offset:9280
	v_exp_f32_e32 v72, v72
	v_exp_f32_e32 v73, v73
	v_cvt_pk_f16_f32 v163, v70, v71
	v_add_f32_e32 v70, v70, v71
	v_add_f32_e32 v231, v231, v68
	v_mfma_f32_32x32x16_f16 v[48:63], v[196:199], v[168:171], v[48:63]
	ds_read_b128 v[196:199], v226 offset:13888
	v_exp_f32_e32 v74, v74
	v_exp_f32_e32 v75, v75
	v_cvt_pk_f16_f32 v164, v72, v73
	v_add_f32_e32 v72, v72, v73
	v_add_f32_e32 v231, v231, v70
	v_mfma_f32_32x32x16_f16 v[32:47], v[200:203], v[172:175], v[32:47]
	ds_read_b128 v[200:203], v226 offset:9312
	v_exp_f32_e32 v76, v76
	v_exp_f32_e32 v77, v77
	v_cvt_pk_f16_f32 v165, v74, v75
	v_add_f32_e32 v74, v74, v75
	v_add_f32_e32 v231, v231, v72
	v_mfma_f32_32x32x16_f16 v[48:63], v[204:207], v[172:175], v[48:63]
	ds_read_b128 v[204:207], v226 offset:13920
	v_exp_f32_e32 v78, v78
	v_exp_f32_e32 v79, v79
	v_cvt_pk_f16_f32 v166, v76, v77
	v_add_f32_e32 v76, v76, v77
	v_add_f32_e32 v231, v231, v74
	v_cvt_pk_f16_f32 v167, v78, v79
	v_add_f32_e32 v78, v78, v79
	v_add_f32_e32 v231, v231, v76
	v_add_f32_e32 v231, v231, v78
	v_cmp_nge_f32_e32 vcc, s34, v231
	s_cbranch_vccnz .Lovf_a11

.Lovfret_b11:
	v_add_f32_e32 v233, v233, v231
	s_waitcnt lgkmcnt(6)
	s_barrier
	s_add_u32 s23, s23, 1
	s_waitcnt vmcnt(8)
	v_cmp_ne_u32_e64 s[20:21], 0, v224
	s_add_u32 s31, s23, 1
	s_and_b32 s31, s31, 31
	s_lshl_b32 s31, s31, 8
	s_add_u32 s26, s31, s22
	s_add_u32 s31, s23, 3
	s_and_b32 s31, s31, 31
	s_mul_i32 s31, s31, 0xc0000
	s_add_u32 s24, s31, s18
	s_add_u32 s25, s31, s19
	s_cmp_eq_u64 s[20:21], -1
	s_cselect_b32 s34, s37, s38
	s_waitcnt lgkmcnt(4)
	v_mfma_f32_32x32x16_f16 v[80:95], v[176:179], v[144:147], v[112:127]
	ds_read_b128 v[176:179], v225 offset:23040
	v_exp_f32_e32 v64, v64
	v_exp_f32_e32 v65, v65
	buffer_load_dword v224, v230, s[8:11], s26 offen
	v_cvt_pk_f16_f32 v208, v208, v209
	v_cvt_pk_f16_f32 v209, v210, v211
	v_mfma_f32_32x32x16_f16 v[80:95], v[180:183], v[148:151], v[80:95]
	ds_read_b128 v[180:183], v225 offset:23072
	v_exp_f32_e32 v66, v66
	v_exp_f32_e32 v67, v67
	v_cvt_pk_f16_f32 v212, v212, v213
	v_cvt_pk_f16_f32 v160, v64, v65
	v_add_f32_e32 v64, v64, v65
	v_cvt_pk_f16_f32 v213, v214, v215
	v_mfma_f32_32x32x16_f16 v[80:95], v[184:187], v[152:155], v[80:95]
	ds_write_b64 v227, v[208:209] offset:0
	ds_write_b64 v227, v[212:213] offset:4608
	ds_read_b128 v[184:187], v225 offset:23104
	v_exp_f32_e32 v68, v68
	v_exp_f32_e32 v69, v69
	v_cvt_pk_f16_f32 v161, v66, v67
	v_add_f32_e32 v66, v66, v67
	v_mfma_f32_32x32x16_f16 v[80:95], v[188:191], v[156:159], v[80:95]
	ds_read_b128 v[188:191], v225 offset:23136
	v_exp_f32_e32 v70, v70
	v_exp_f32_e32 v71, v71
	v_cvt_pk_f16_f32 v162, v68, v69
	v_add_f32_e32 v68, v68, v69
	v_add_f32_e32 v231, v64, v66
	s_waitcnt lgkmcnt(6)
	v_mfma_f32_32x32x16_f16 v[32:47], v[192:195], v[168:171], v[32:47]
	ds_read_b128 v[192:195], v226 offset:18432
	v_exp_f32_e32 v72, v72
	v_exp_f32_e32 v73, v73
	v_cvt_pk_f16_f32 v163, v70, v71
	v_add_f32_e32 v70, v70, v71
	v_add_f32_e32 v231, v231, v68
	v_mfma_f32_32x32x16_f16 v[48:63], v[196:199], v[168:171], v[48:63]
	ds_read_b128 v[196:199], v226 offset:23040
	v_exp_f32_e32 v74, v74
	v_exp_f32_e32 v75, v75
	v_cvt_pk_f16_f32 v164, v72, v73
	v_add_f32_e32 v72, v72, v73
	v_add_f32_e32 v231, v231, v70
	v_mfma_f32_32x32x16_f16 v[32:47], v[200:203], v[172:175], v[32:47]
	ds_read_b128 v[200:203], v226 offset:18464
	v_exp_f32_e32 v76, v76
	v_exp_f32_e32 v77, v77
	v_cvt_pk_f16_f32 v165, v74, v75
	v_add_f32_e32 v74, v74, v75
	v_add_f32_e32 v231, v231, v72
	v_mfma_f32_32x32x16_f16 v[48:63], v[204:207], v[172:175], v[48:63]
	ds_read_b128 v[204:207], v226 offset:23072
	v_exp_f32_e32 v78, v78
	v_exp_f32_e32 v79, v79
	v_cvt_pk_f16_f32 v166, v76, v77
	v_add_f32_e32 v76, v76, v77
	v_add_f32_e32 v231, v231, v74
	v_cvt_pk_f16_f32 v167, v78, v79
	v_add_f32_e32 v78, v78, v79
	v_add_f32_e32 v231, v231, v76
	v_add_f32_e32 v231, v231, v78
	v_cmp_nge_f32_e32 vcc, s34, v231
	s_cbranch_vccnz .Lovf_a20

.Lovfret_b20:
	v_add_f32_e32 v233, v233, v231
	s_waitcnt lgkmcnt(4)
	v_mfma_f32_32x32x16_f16 v[80:95], v[176:179], v[144:147], v[112:127]
	ds_read_b128 v[176:179], v225 offset:27648
	v_exp_f32_e32 v64, v64
	v_exp_f32_e32 v65, v65
	s_waitcnt vmcnt(3)
	v_cvt_pk_f16_f32 v216, v216, v217
	v_cvt_pk_f16_f32 v217, v218, v219
	v_mfma_f32_32x32x16_f16 v[80:95], v[180:183], v[148:151], v[80:95]
	ds_read_b128 v[180:183], v225 offset:27680
	v_exp_f32_e32 v66, v66
	v_exp_f32_e32 v67, v67
	v_cvt_pk_f16_f32 v218, v220, v221
	v_cvt_pk_f16_f32 v160, v64, v65
	v_add_f32_e32 v64, v64, v65
	v_cvt_pk_f16_f32 v219, v222, v223
	v_mfma_f32_32x32x16_f16 v[80:95], v[184:187], v[152:155], v[80:95]
	ds_write_b128 v228, v[216:219] offset:0
	ds_read_b128 v[184:187], v225 offset:27712
	v_exp_f32_e32 v68, v68
	v_exp_f32_e32 v69, v69
	v_cvt_pk_f16_f32 v161, v66, v67
	v_add_f32_e32 v66, v66, v67
	v_mfma_f32_32x32x16_f16 v[80:95], v[188:191], v[156:159], v[80:95]
	ds_read_b128 v[188:191], v225 offset:27744
	v_exp_f32_e32 v70, v70
	v_exp_f32_e32 v71, v71
	v_cvt_pk_f16_f32 v162, v68, v69
	v_add_f32_e32 v68, v68, v69
	v_add_f32_e32 v231, v64, v66
	s_waitcnt lgkmcnt(5)
	v_mfma_f32_32x32x16_f16 v[32:47], v[192:195], v[168:171], v[32:47]
	ds_read_b128 v[192:195], v226 offset:18496
	v_exp_f32_e32 v72, v72
	v_exp_f32_e32 v73, v73
	v_cvt_pk_f16_f32 v163, v70, v71
	v_add_f32_e32 v70, v70, v71
	v_add_f32_e32 v231, v231, v68
	v_mfma_f32_32x32x16_f16 v[48:63], v[196:199], v[168:171], v[48:63]
	ds_read_b128 v[196:199], v226 offset:23104
	v_exp_f32_e32 v74, v74
	v_exp_f32_e32 v75, v75
	v_cvt_pk_f16_f32 v164, v72, v73
	v_add_f32_e32 v72, v72, v73
	v_add_f32_e32 v231, v231, v70
	v_mfma_f32_32x32x16_f16 v[32:47], v[200:203], v[172:175], v[32:47]
	ds_read_b128 v[200:203], v226 offset:18528
	v_exp_f32_e32 v76, v76
	v_exp_f32_e32 v77, v77
	v_cvt_pk_f16_f32 v165, v74, v75
	v_add_f32_e32 v74, v74, v75
	v_add_f32_e32 v231, v231, v72
	v_mfma_f32_32x32x16_f16 v[48:63], v[204:207], v[172:175], v[48:63]
	ds_read_b128 v[204:207], v226 offset:23136
	v_exp_f32_e32 v78, v78
	v_exp_f32_e32 v79, v79
	v_cvt_pk_f16_f32 v166, v76, v77
	v_add_f32_e32 v76, v76, v77
	v_add_f32_e32 v231, v231, v74
	v_cvt_pk_f16_f32 v167, v78, v79
	v_add_f32_e32 v78, v78, v79
	v_add_f32_e32 v231, v231, v76
	v_add_f32_e32 v231, v231, v78
	v_cmp_nge_f32_e32 vcc, s34, v231
	s_cbranch_vccnz .Lovf_a21

.Lovfret_b21:
	v_add_f32_e32 v233, v233, v231
	s_waitcnt lgkmcnt(6)
	s_barrier
	s_add_u32 s23, s23, 1
	s_waitcnt vmcnt(8)
	v_cmp_ne_u32_e64 s[20:21], 0, v224
	s_add_u32 s31, s23, 1
	s_and_b32 s31, s31, 31
	s_lshl_b32 s31, s31, 8
	s_add_u32 s26, s31, s22
	s_add_u32 s31, s23, 3
	s_and_b32 s31, s31, 31
	s_mul_i32 s31, s31, 0xc0000
	s_add_u32 s24, s31, s18
	s_add_u32 s25, s31, s19
	s_cmp_eq_u64 s[20:21], -1
	s_cselect_b32 s34, s37, s38
	s_waitcnt lgkmcnt(4)
	v_mfma_f32_32x32x16_f16 v[80:95], v[176:179], v[144:147], v[112:127]
	ds_read_b128 v[176:179], v225 offset:32256
	v_exp_f32_e32 v64, v64
	v_exp_f32_e32 v65, v65
	buffer_load_dword v224, v230, s[8:11], s26 offen
	v_cvt_pk_f16_f32 v208, v208, v209
	v_cvt_pk_f16_f32 v209, v210, v211
	v_mfma_f32_32x32x16_f16 v[80:95], v[180:183], v[148:151], v[80:95]
	ds_read_b128 v[180:183], v225 offset:32288
	v_exp_f32_e32 v66, v66
	v_exp_f32_e32 v67, v67
	v_cvt_pk_f16_f32 v212, v212, v213
	v_cvt_pk_f16_f32 v160, v64, v65
	v_add_f32_e32 v64, v64, v65
	v_cvt_pk_f16_f32 v213, v214, v215
	v_mfma_f32_32x32x16_f16 v[80:95], v[184:187], v[152:155], v[80:95]
	ds_write_b64 v227, v[208:209] offset:9216
	ds_write_b64 v227, v[212:213] offset:13824
	ds_read_b128 v[184:187], v225 offset:32320
	v_exp_f32_e32 v68, v68
	v_exp_f32_e32 v69, v69
	v_cvt_pk_f16_f32 v161, v66, v67
	v_add_f32_e32 v66, v66, v67
	v_mfma_f32_32x32x16_f16 v[80:95], v[188:191], v[156:159], v[80:95]
	ds_read_b128 v[188:191], v225 offset:32352
	v_exp_f32_e32 v70, v70
	v_exp_f32_e32 v71, v71
	v_cvt_pk_f16_f32 v162, v68, v69
	v_add_f32_e32 v68, v68, v69
	v_add_f32_e32 v231, v64, v66
	s_waitcnt lgkmcnt(6)
	v_mfma_f32_32x32x16_f16 v[32:47], v[192:195], v[168:171], v[32:47]
	ds_read_b128 v[192:195], v226 offset:27648
	v_exp_f32_e32 v72, v72
	v_exp_f32_e32 v73, v73
	v_cvt_pk_f16_f32 v163, v70, v71
	v_add_f32_e32 v70, v70, v71
	v_add_f32_e32 v231, v231, v68
	v_mfma_f32_32x32x16_f16 v[48:63], v[196:199], v[168:171], v[48:63]
	ds_read_b128 v[196:199], v226 offset:32256
	v_exp_f32_e32 v74, v74
	v_exp_f32_e32 v75, v75
	v_cvt_pk_f16_f32 v164, v72, v73
	v_add_f32_e32 v72, v72, v73
	v_add_f32_e32 v231, v231, v70
	v_mfma_f32_32x32x16_f16 v[32:47], v[200:203], v[172:175], v[32:47]
	ds_read_b128 v[200:203], v226 offset:27680
	v_exp_f32_e32 v76, v76
	v_exp_f32_e32 v77, v77
	v_cvt_pk_f16_f32 v165, v74, v75
	v_add_f32_e32 v74, v74, v75
	v_add_f32_e32 v231, v231, v72
	v_mfma_f32_32x32x16_f16 v[48:63], v[204:207], v[172:175], v[48:63]
	ds_read_b128 v[204:207], v226 offset:32288
	v_exp_f32_e32 v78, v78
	v_exp_f32_e32 v79, v79
	v_cvt_pk_f16_f32 v166, v76, v77
	v_add_f32_e32 v76, v76, v77
	v_add_f32_e32 v231, v231, v74
	v_cvt_pk_f16_f32 v167, v78, v79
	v_add_f32_e32 v78, v78, v79
	v_add_f32_e32 v231, v231, v76
	v_add_f32_e32 v231, v231, v78
	v_cmp_nge_f32_e32 vcc, s34, v231
	s_cbranch_vccnz .Lovf_a30

.Lovfret_b30:
	v_add_f32_e32 v233, v233, v231
	s_waitcnt lgkmcnt(4)
	v_mfma_f32_32x32x16_f16 v[80:95], v[176:179], v[144:147], v[112:127]
	ds_read_b128 v[176:179], v225 offset:0
	v_exp_f32_e32 v64, v64
	v_exp_f32_e32 v65, v65
	s_waitcnt vmcnt(3)
	v_cvt_pk_f16_f32 v216, v216, v217
	v_cvt_pk_f16_f32 v217, v218, v219
	v_mfma_f32_32x32x16_f16 v[80:95], v[180:183], v[148:151], v[80:95]
	ds_read_b128 v[180:183], v225 offset:32
	v_exp_f32_e32 v66, v66
	v_exp_f32_e32 v67, v67
	v_cvt_pk_f16_f32 v218, v220, v221
	v_cvt_pk_f16_f32 v160, v64, v65
	v_add_f32_e32 v64, v64, v65
	v_cvt_pk_f16_f32 v219, v222, v223
	v_mfma_f32_32x32x16_f16 v[80:95], v[184:187], v[152:155], v[80:95]
	ds_write_b128 v228, v[216:219] offset:9216
	ds_read_b128 v[184:187], v225 offset:64
	v_exp_f32_e32 v68, v68
	v_exp_f32_e32 v69, v69
	v_cvt_pk_f16_f32 v161, v66, v67
	v_add_f32_e32 v66, v66, v67
	v_mfma_f32_32x32x16_f16 v[80:95], v[188:191], v[156:159], v[80:95]
	ds_read_b128 v[188:191], v225 offset:96
	v_exp_f32_e32 v70, v70
	v_exp_f32_e32 v71, v71
	v_cvt_pk_f16_f32 v162, v68, v69
	v_add_f32_e32 v68, v68, v69
	v_add_f32_e32 v231, v64, v66
	s_waitcnt lgkmcnt(5)
	v_mfma_f32_32x32x16_f16 v[32:47], v[192:195], v[168:171], v[32:47]
	ds_read_b128 v[192:195], v226 offset:27712
	v_exp_f32_e32 v72, v72
	v_exp_f32_e32 v73, v73
	v_cvt_pk_f16_f32 v163, v70, v71
	v_add_f32_e32 v70, v70, v71
	v_add_f32_e32 v231, v231, v68
	v_mfma_f32_32x32x16_f16 v[48:63], v[196:199], v[168:171], v[48:63]
	ds_read_b128 v[196:199], v226 offset:32320
	v_exp_f32_e32 v74, v74
	v_exp_f32_e32 v75, v75
	v_cvt_pk_f16_f32 v164, v72, v73
	v_add_f32_e32 v72, v72, v73
	v_add_f32_e32 v231, v231, v70
	v_mfma_f32_32x32x16_f16 v[32:47], v[200:203], v[172:175], v[32:47]
	ds_read_b128 v[200:203], v226 offset:27744
	v_exp_f32_e32 v76, v76
	v_exp_f32_e32 v77, v77
	v_cvt_pk_f16_f32 v165, v74, v75
	v_add_f32_e32 v74, v74, v75
	v_add_f32_e32 v231, v231, v72
	v_mfma_f32_32x32x16_f16 v[48:63], v[204:207], v[172:175], v[48:63]
	ds_read_b128 v[204:207], v226 offset:32352
	v_exp_f32_e32 v78, v78
	v_exp_f32_e32 v79, v79
	v_cvt_pk_f16_f32 v166, v76, v77
	v_add_f32_e32 v76, v76, v77
	v_add_f32_e32 v231, v231, v74
	v_cvt_pk_f16_f32 v167, v78, v79
	v_add_f32_e32 v78, v78, v79
	v_add_f32_e32 v231, v231, v76
	v_add_f32_e32 v231, v231, v78
	v_cmp_nge_f32_e32 vcc, s34, v231
	s_cbranch_vccnz .Lovf_a31

.Lovfret_b31:
	v_add_f32_e32 v233, v233, v231
	s_waitcnt lgkmcnt(6)
	s_barrier
	s_add_u32 s23, s23, 1
	s_add_u32 s27, s27, 1
	s_cmp_eq_u32 s27, 8
	s_cbranch_scc0 .Lbody
	s_waitcnt lgkmcnt(0)
	v_mfma_f32_32x32x16_f16 v[32:47], v[192:195], v[168:171], v[32:47]
	v_mfma_f32_32x32x16_f16 v[48:63], v[196:199], v[168:171], v[48:63]
	v_mfma_f32_32x32x16_f16 v[32:47], v[200:203], v[172:175], v[32:47]
	v_mfma_f32_32x32x16_f16 v[48:63], v[204:207], v[172:175], v[48:63]
	s_nop 15
	s_nop 7
	v_mov_b32_e32 v235, v232
	v_mov_b32_e32 v236, v232
	s_nop 1
	v_permlane32_swap_b32_e32 v235, v236
	v_add_f32_e32 v236, v235, v236
	v_rcp_f32_e32 v237, v236
	s_nop 0
	v_fma_f32 v238, -v236, v237, 1.0
	v_fmac_f32_e32 v237, v238, v237
	v_mul_f32_e32 v0, v237, v0
	v_mul_f32_e32 v1, v237, v1
	v_mul_f32_e32 v2, v237, v2
	v_mul_f32_e32 v3, v237, v3
	v_mul_f32_e32 v4, v237, v4
	v_mul_f32_e32 v5, v237, v5
	v_mul_f32_e32 v6, v237, v6
	v_mul_f32_e32 v7, v237, v7
	v_mul_f32_e32 v8, v237, v8
	v_mul_f32_e32 v9, v237, v9
	v_mul_f32_e32 v10, v237, v10
	v_mul_f32_e32 v11, v237, v11
	v_mul_f32_e32 v12, v237, v12
	v_mul_f32_e32 v13, v237, v13
	v_mul_f32_e32 v14, v237, v14
	v_mul_f32_e32 v15, v237, v15
	v_mul_f32_e32 v16, v237, v16
	v_mul_f32_e32 v17, v237, v17
	v_mul_f32_e32 v18, v237, v18
	v_mul_f32_e32 v19, v237, v19
	v_mul_f32_e32 v20, v237, v20
	v_mul_f32_e32 v21, v237, v21
	v_mul_f32_e32 v22, v237, v22
	v_mul_f32_e32 v23, v237, v23
	v_mul_f32_e32 v24, v237, v24
	v_mul_f32_e32 v25, v237, v25
	v_mul_f32_e32 v26, v237, v26
	v_mul_f32_e32 v27, v237, v27
	v_mul_f32_e32 v28, v237, v28
	v_mul_f32_e32 v29, v237, v29
	v_mul_f32_e32 v30, v237, v30
	v_mul_f32_e32 v31, v237, v31
	ds_write_b128 v241, v[0:3] offset:0
	ds_write_b128 v241, v[16:19] offset:128
	ds_write_b128 v241, v[4:7] offset:32
	ds_write_b128 v241, v[20:23] offset:160
	ds_write_b128 v241, v[8:11] offset:64
	ds_write_b128 v241, v[24:27] offset:192
	ds_write_b128 v241, v[12:15] offset:96
	ds_write_b128 v241, v[28:31] offset:224
	s_waitcnt lgkmcnt(0)
	ds_read_b128 v[0:3], v242 offset:0
	ds_read_b128 v[4:7], v242 offset:1088
	ds_read_b128 v[8:11], v242 offset:2176
	ds_read_b128 v[12:15], v242 offset:3264
	ds_read_b128 v[16:19], v242 offset:4352
	ds_read_b128 v[20:23], v242 offset:5440
	ds_read_b128 v[24:27], v242 offset:6528
	ds_read_b128 v[28:31], v242 offset:7616
	s_waitcnt lgkmcnt(7)
	s_add_u32 s31, s30, 0x0
	buffer_store_dwordx4 v[0:3], v244, s[12:15], s31 offen nt sc1
	s_waitcnt lgkmcnt(6)
	s_add_u32 s31, s30, 0x4000
	buffer_store_dwordx4 v[4:7], v244, s[12:15], s31 offen nt sc1
	s_waitcnt lgkmcnt(5)
	s_add_u32 s31, s30, 0x8000
	buffer_store_dwordx4 v[8:11], v244, s[12:15], s31 offen nt sc1
	s_waitcnt lgkmcnt(4)
	s_add_u32 s31, s30, 0xc000
	buffer_store_dwordx4 v[12:15], v244, s[12:15], s31 offen nt sc1
	s_waitcnt lgkmcnt(3)
	s_add_u32 s31, s30, 0x10000
	buffer_store_dwordx4 v[16:19], v244, s[12:15], s31 offen nt sc1
	s_waitcnt lgkmcnt(2)
	s_add_u32 s31, s30, 0x14000
	buffer_store_dwordx4 v[20:23], v244, s[12:15], s31 offen nt sc1
	s_waitcnt lgkmcnt(1)
	s_add_u32 s31, s30, 0x18000
	buffer_store_dwordx4 v[24:27], v244, s[12:15], s31 offen nt sc1
	s_waitcnt lgkmcnt(0)
	s_add_u32 s31, s30, 0x1c000
	buffer_store_dwordx4 v[28:31], v244, s[12:15], s31 offen nt sc1
	v_mov_b32_e32 v235, v233
	v_mov_b32_e32 v236, v233
	s_nop 1
	v_permlane32_swap_b32_e32 v235, v236
	v_add_f32_e32 v236, v235, v236
	v_rcp_f32_e32 v237, v236
	s_nop 0
	v_fma_f32 v238, -v236, v237, 1.0
	v_fmac_f32_e32 v237, v238, v237
	v_mul_f32_e32 v32, v237, v32
	v_mul_f32_e32 v33, v237, v33
	v_mul_f32_e32 v34, v237, v34
	v_mul_f32_e32 v35, v237, v35
	v_mul_f32_e32 v36, v237, v36
	v_mul_f32_e32 v37, v237, v37
	v_mul_f32_e32 v38, v237, v38
	v_mul_f32_e32 v39, v237, v39
	v_mul_f32_e32 v40, v237, v40
	v_mul_f32_e32 v41, v237, v41
	v_mul_f32_e32 v42, v237, v42
	v_mul_f32_e32 v43, v237, v43
	v_mul_f32_e32 v44, v237, v44
	v_mul_f32_e32 v45, v237, v45
	v_mul_f32_e32 v46, v237, v46
	v_mul_f32_e32 v47, v237, v47
	v_mul_f32_e32 v48, v237, v48
	v_mul_f32_e32 v49, v237, v49
	v_mul_f32_e32 v50, v237, v50
	v_mul_f32_e32 v51, v237, v51
	v_mul_f32_e32 v52, v237, v52
	v_mul_f32_e32 v53, v237, v53
	v_mul_f32_e32 v54, v237, v54
	v_mul_f32_e32 v55, v237, v55
	v_mul_f32_e32 v56, v237, v56
	v_mul_f32_e32 v57, v237, v57
	v_mul_f32_e32 v58, v237, v58
	v_mul_f32_e32 v59, v237, v59
	v_mul_f32_e32 v60, v237, v60
	v_mul_f32_e32 v61, v237, v61
	v_mul_f32_e32 v62, v237, v62
	v_mul_f32_e32 v63, v237, v63
	ds_write_b128 v241, v[32:35] offset:0
	ds_write_b128 v241, v[48:51] offset:128
	ds_write_b128 v241, v[36:39] offset:32
	ds_write_b128 v241, v[52:55] offset:160
	ds_write_b128 v241, v[40:43] offset:64
	ds_write_b128 v241, v[56:59] offset:192
	ds_write_b128 v241, v[44:47] offset:96
	ds_write_b128 v241, v[60:63] offset:224
	s_waitcnt lgkmcnt(0)
	ds_read_b128 v[32:35], v242 offset:0
	ds_read_b128 v[36:39], v242 offset:1088
	ds_read_b128 v[40:43], v242 offset:2176
	ds_read_b128 v[44:47], v242 offset:3264
	ds_read_b128 v[48:51], v242 offset:4352
	ds_read_b128 v[52:55], v242 offset:5440
	ds_read_b128 v[56:59], v242 offset:6528
	ds_read_b128 v[60:63], v242 offset:7616
	s_waitcnt lgkmcnt(7)
	s_add_u32 s31, s30, 0x400000
	buffer_store_dwordx4 v[32:35], v244, s[12:15], s31 offen nt sc1
	s_waitcnt lgkmcnt(6)
	s_add_u32 s31, s30, 0x404000
	buffer_store_dwordx4 v[36:39], v244, s[12:15], s31 offen nt sc1
	s_waitcnt lgkmcnt(5)
	s_add_u32 s31, s30, 0x408000
	buffer_store_dwordx4 v[40:43], v244, s[12:15], s31 offen nt sc1
	s_waitcnt lgkmcnt(4)
	s_add_u32 s31, s30, 0x40c000
	buffer_store_dwordx4 v[44:47], v244, s[12:15], s31 offen nt sc1
	s_waitcnt lgkmcnt(3)
	s_add_u32 s31, s30, 0x410000
	buffer_store_dwordx4 v[48:51], v244, s[12:15], s31 offen nt sc1
	s_waitcnt lgkmcnt(2)
	s_add_u32 s31, s30, 0x414000
	buffer_store_dwordx4 v[52:55], v244, s[12:15], s31 offen nt sc1
	s_waitcnt lgkmcnt(1)
	s_add_u32 s31, s30, 0x418000
	buffer_store_dwordx4 v[56:59], v244, s[12:15], s31 offen nt sc1
	s_waitcnt lgkmcnt(0)
	s_add_u32 s31, s30, 0x41c000
	buffer_store_dwordx4 v[60:63], v244, s[12:15], s31 offen nt sc1
	s_endpgm
.Lovf_a00:
	s_waitcnt lgkmcnt(0)
	s_nop 15
	s_nop 15
	s_nop 15
	ds_read_b128 v[168:171], v225 offset:0
	ds_read_b128 v[172:175], v225 offset:32
	s_waitcnt lgkmcnt(0)
	v_mfma_f32_32x32x16_f16 v[64:79], v[168:171], v[128:131], v[96:111]
	v_mfma_f32_32x32x16_f16 v[64:79], v[172:175], v[132:135], v[64:79]
	s_nop 15
	ds_read_b128 v[168:171], v225 offset:64
	ds_read_b128 v[172:175], v225 offset:96
	s_waitcnt lgkmcnt(0)
	v_mfma_f32_32x32x16_f16 v[64:79], v[168:171], v[136:139], v[64:79]
	v_mfma_f32_32x32x16_f16 v[64:79], v[172:175], v[140:143], v[64:79]
	s_nop 15
	s_nop 15
	s_cmp_eq_u64 s[20:21], -1
	s_cbranch_scc1 .Lovfnm_a00
	v_lshrrev_b32_e64 v235, v234, s20
	v_bfe_u32 v236, v235, 0, 1
	v_cvt_f32_u32_e32 v236, v236
	v_sub_f32_e32 v236, 1.0, v236
	v_fmac_f32_e32 v64, s35, v236
	v_bfe_u32 v236, v235, 1, 1
	v_cvt_f32_u32_e32 v236, v236
	v_sub_f32_e32 v236, 1.0, v236
	v_fmac_f32_e32 v65, s35, v236
	v_bfe_u32 v236, v235, 2, 1
	v_cvt_f32_u32_e32 v236, v236
	v_sub_f32_e32 v236, 1.0, v236
	v_fmac_f32_e32 v66, s35, v236
	v_bfe_u32 v236, v235, 3, 1
	v_cvt_f32_u32_e32 v236, v236
	v_sub_f32_e32 v236, 1.0, v236
	v_fmac_f32_e32 v67, s35, v236
	v_bfe_u32 v236, v235, 8, 1
	v_cvt_f32_u32_e32 v236, v236
	v_sub_f32_e32 v236, 1.0, v236
	v_fmac_f32_e32 v68, s35, v236
	v_bfe_u32 v236, v235, 9, 1
	v_cvt_f32_u32_e32 v236, v236
	v_sub_f32_e32 v236, 1.0, v236
	v_fmac_f32_e32 v69, s35, v236
	v_bfe_u32 v236, v235, 10, 1
	v_cvt_f32_u32_e32 v236, v236
	v_sub_f32_e32 v236, 1.0, v236
	v_fmac_f32_e32 v70, s35, v236
	v_bfe_u32 v236, v235, 11, 1
	v_cvt_f32_u32_e32 v236, v236
	v_sub_f32_e32 v236, 1.0, v236
	v_fmac_f32_e32 v71, s35, v236
	v_bfe_u32 v236, v235, 16, 1
	v_cvt_f32_u32_e32 v236, v236
	v_sub_f32_e32 v236, 1.0, v236
	v_fmac_f32_e32 v72, s35, v236
	v_bfe_u32 v236, v235, 17, 1
	v_cvt_f32_u32_e32 v236, v236
	v_sub_f32_e32 v236, 1.0, v236
	v_fmac_f32_e32 v73, s35, v236
	v_bfe_u32 v236, v235, 18, 1
	v_cvt_f32_u32_e32 v236, v236
	v_sub_f32_e32 v236, 1.0, v236
	v_fmac_f32_e32 v74, s35, v236
	v_bfe_u32 v236, v235, 19, 1
	v_cvt_f32_u32_e32 v236, v236
	v_sub_f32_e32 v236, 1.0, v236
	v_fmac_f32_e32 v75, s35, v236
	v_bfe_u32 v236, v235, 24, 1
	v_cvt_f32_u32_e32 v236, v236
	v_sub_f32_e32 v236, 1.0, v236
	v_fmac_f32_e32 v76, s35, v236
	v_bfe_u32 v236, v235, 25, 1
	v_cvt_f32_u32_e32 v236, v236
	v_sub_f32_e32 v236, 1.0, v236
	v_fmac_f32_e32 v77, s35, v236
	v_bfe_u32 v236, v235, 26, 1
	v_cvt_f32_u32_e32 v236, v236
	v_sub_f32_e32 v236, 1.0, v236
	v_fmac_f32_e32 v78, s35, v236
	v_bfe_u32 v236, v235, 27, 1
	v_cvt_f32_u32_e32 v236, v236
	v_sub_f32_e32 v236, 1.0, v236
	v_fmac_f32_e32 v79, s35, v236
.Lovfnm_a00:
	v_max3_f32 v235, v64, v65, v66
	v_max3_f32 v235, v235, v67, v68
	v_max3_f32 v235, v235, v69, v70
	v_max3_f32 v235, v235, v71, v72
	v_max3_f32 v235, v235, v73, v74
	v_max3_f32 v235, v235, v75, v76
	v_max3_f32 v235, v235, v77, v78
	v_max_f32_e32 v235, v235, v79
	v_mov_b32_e32 v236, v235
	s_nop 1
	v_permlane32_swap_b32_e32 v235, v236
	v_max_f32_e32 v235, v235, v236
	v_max_f32_e32 v235, 0, v235
	v_exp_f32_e64 v237, -v235
	v_sub_f32_e32 v96, v96, v235
	v_sub_f32_e32 v97, v97, v235
	v_sub_f32_e32 v98, v98, v235
	v_sub_f32_e32 v99, v99, v235
	v_sub_f32_e32 v100, v100, v235
	v_sub_f32_e32 v101, v101, v235
	v_sub_f32_e32 v102, v102, v235
	v_sub_f32_e32 v103, v103, v235
	v_sub_f32_e32 v104, v104, v235
	v_sub_f32_e32 v105, v105, v235
	v_sub_f32_e32 v106, v106, v235
	v_sub_f32_e32 v107, v107, v235
	v_sub_f32_e32 v108, v108, v235
	v_sub_f32_e32 v109, v109, v235
	v_sub_f32_e32 v110, v110, v235
	v_sub_f32_e32 v111, v111, v235
	v_mul_f32_e32 v232, v232, v237
	v_mul_f32_e32 v0, v0, v237
	v_mul_f32_e32 v1, v1, v237
	v_mul_f32_e32 v2, v2, v237
	v_mul_f32_e32 v3, v3, v237
	v_mul_f32_e32 v4, v4, v237
	v_mul_f32_e32 v5, v5, v237
	v_mul_f32_e32 v6, v6, v237
	v_mul_f32_e32 v7, v7, v237
	v_mul_f32_e32 v8, v8, v237
	v_mul_f32_e32 v9, v9, v237
	v_mul_f32_e32 v10, v10, v237
	v_mul_f32_e32 v11, v11, v237
	v_mul_f32_e32 v12, v12, v237
	v_mul_f32_e32 v13, v13, v237
	v_mul_f32_e32 v14, v14, v237
	v_mul_f32_e32 v15, v15, v237
	v_mul_f32_e32 v16, v16, v237
	v_mul_f32_e32 v17, v17, v237
	v_mul_f32_e32 v18, v18, v237
	v_mul_f32_e32 v19, v19, v237
	v_mul_f32_e32 v20, v20, v237
	v_mul_f32_e32 v21, v21, v237
	v_mul_f32_e32 v22, v22, v237
	v_mul_f32_e32 v23, v23, v237
	v_mul_f32_e32 v24, v24, v237
	v_mul_f32_e32 v25, v25, v237
	v_mul_f32_e32 v26, v26, v237
	v_mul_f32_e32 v27, v27, v237
	v_mul_f32_e32 v28, v28, v237
	v_mul_f32_e32 v29, v29, v237
	v_mul_f32_e32 v30, v30, v237
	v_mul_f32_e32 v31, v31, v237
	v_sub_f32_e32 v64, v64, v235
	v_sub_f32_e32 v65, v65, v235
	v_sub_f32_e32 v66, v66, v235
	v_sub_f32_e32 v67, v67, v235
	v_sub_f32_e32 v68, v68, v235
	v_sub_f32_e32 v69, v69, v235
	v_sub_f32_e32 v70, v70, v235
	v_sub_f32_e32 v71, v71, v235
	v_sub_f32_e32 v72, v72, v235
	v_sub_f32_e32 v73, v73, v235
	v_sub_f32_e32 v74, v74, v235
	v_sub_f32_e32 v75, v75, v235
	v_sub_f32_e32 v76, v76, v235
	v_sub_f32_e32 v77, v77, v235
	v_sub_f32_e32 v78, v78, v235
	v_sub_f32_e32 v79, v79, v235
	v_exp_f32_e32 v64, v64
	v_exp_f32_e32 v65, v65
	v_exp_f32_e32 v66, v66
	v_exp_f32_e32 v67, v67
	v_exp_f32_e32 v68, v68
	v_exp_f32_e32 v69, v69
	v_exp_f32_e32 v70, v70
	v_exp_f32_e32 v71, v71
	v_exp_f32_e32 v72, v72
	v_exp_f32_e32 v73, v73
	v_exp_f32_e32 v74, v74
	v_exp_f32_e32 v75, v75
	v_exp_f32_e32 v76, v76
	v_exp_f32_e32 v77, v77
	v_exp_f32_e32 v78, v78
	v_exp_f32_e32 v79, v79
	s_nop 0
	v_add_f32_e32 v231, v64, v65
	v_add_f32_e32 v231, v231, v66
	v_add_f32_e32 v231, v231, v67
	v_add_f32_e32 v231, v231, v68
	v_add_f32_e32 v231, v231, v69
	v_add_f32_e32 v231, v231, v70
	v_add_f32_e32 v231, v231, v71
	v_add_f32_e32 v231, v231, v72
	v_add_f32_e32 v231, v231, v73
	v_add_f32_e32 v231, v231, v74
	v_add_f32_e32 v231, v231, v75
	v_add_f32_e32 v231, v231, v76
	v_add_f32_e32 v231, v231, v77
	v_add_f32_e32 v231, v231, v78
	v_add_f32_e32 v231, v231, v79
	v_cvt_pk_f16_f32 v160, v64, v65
	v_cvt_pk_f16_f32 v161, v66, v67
	v_cvt_pk_f16_f32 v162, v68, v69
	v_cvt_pk_f16_f32 v163, v70, v71
	v_cvt_pk_f16_f32 v164, v72, v73
	v_cvt_pk_f16_f32 v165, v74, v75
	v_cvt_pk_f16_f32 v166, v76, v77
	v_cvt_pk_f16_f32 v167, v78, v79
	s_branch .Lovfret_a00
.Lovf_b00:
	s_waitcnt lgkmcnt(0)
	s_nop 15
	s_nop 15
	s_nop 15
	ds_read_b128 v[160:163], v225 offset:0
	ds_read_b128 v[164:167], v225 offset:32
	s_waitcnt lgkmcnt(0)
	v_mfma_f32_32x32x16_f16 v[80:95], v[160:163], v[144:147], v[112:127]
	v_mfma_f32_32x32x16_f16 v[80:95], v[164:167], v[148:151], v[80:95]
	s_nop 15
	ds_read_b128 v[160:163], v225 offset:64
	ds_read_b128 v[164:167], v225 offset:96
	s_waitcnt lgkmcnt(0)
	v_mfma_f32_32x32x16_f16 v[80:95], v[160:163], v[152:155], v[80:95]
	v_mfma_f32_32x32x16_f16 v[80:95], v[164:167], v[156:159], v[80:95]
	s_nop 15
	s_nop 15
	s_cmp_eq_u64 s[20:21], -1
	s_cbranch_scc1 .Lovfnm_b00
	v_lshrrev_b32_e64 v235, v234, s20
	v_bfe_u32 v236, v235, 0, 1
	v_cvt_f32_u32_e32 v236, v236
	v_sub_f32_e32 v236, 1.0, v236
	v_fmac_f32_e32 v80, s35, v236
	v_bfe_u32 v236, v235, 1, 1
	v_cvt_f32_u32_e32 v236, v236
	v_sub_f32_e32 v236, 1.0, v236
	v_fmac_f32_e32 v81, s35, v236
	v_bfe_u32 v236, v235, 2, 1
	v_cvt_f32_u32_e32 v236, v236
	v_sub_f32_e32 v236, 1.0, v236
	v_fmac_f32_e32 v82, s35, v236
	v_bfe_u32 v236, v235, 3, 1
	v_cvt_f32_u32_e32 v236, v236
	v_sub_f32_e32 v236, 1.0, v236
	v_fmac_f32_e32 v83, s35, v236
	v_bfe_u32 v236, v235, 8, 1
	v_cvt_f32_u32_e32 v236, v236
	v_sub_f32_e32 v236, 1.0, v236
	v_fmac_f32_e32 v84, s35, v236
	v_bfe_u32 v236, v235, 9, 1
	v_cvt_f32_u32_e32 v236, v236
	v_sub_f32_e32 v236, 1.0, v236
	v_fmac_f32_e32 v85, s35, v236
	v_bfe_u32 v236, v235, 10, 1
	v_cvt_f32_u32_e32 v236, v236
	v_sub_f32_e32 v236, 1.0, v236
	v_fmac_f32_e32 v86, s35, v236
	v_bfe_u32 v236, v235, 11, 1
	v_cvt_f32_u32_e32 v236, v236
	v_sub_f32_e32 v236, 1.0, v236
	v_fmac_f32_e32 v87, s35, v236
	v_bfe_u32 v236, v235, 16, 1
	v_cvt_f32_u32_e32 v236, v236
	v_sub_f32_e32 v236, 1.0, v236
	v_fmac_f32_e32 v88, s35, v236
	v_bfe_u32 v236, v235, 17, 1
	v_cvt_f32_u32_e32 v236, v236
	v_sub_f32_e32 v236, 1.0, v236
	v_fmac_f32_e32 v89, s35, v236
	v_bfe_u32 v236, v235, 18, 1
	v_cvt_f32_u32_e32 v236, v236
	v_sub_f32_e32 v236, 1.0, v236
	v_fmac_f32_e32 v90, s35, v236
	v_bfe_u32 v236, v235, 19, 1
	v_cvt_f32_u32_e32 v236, v236
	v_sub_f32_e32 v236, 1.0, v236
	v_fmac_f32_e32 v91, s35, v236
	v_bfe_u32 v236, v235, 24, 1
	v_cvt_f32_u32_e32 v236, v236
	v_sub_f32_e32 v236, 1.0, v236
	v_fmac_f32_e32 v92, s35, v236
	v_bfe_u32 v236, v235, 25, 1
	v_cvt_f32_u32_e32 v236, v236
	v_sub_f32_e32 v236, 1.0, v236
	v_fmac_f32_e32 v93, s35, v236
	v_bfe_u32 v236, v235, 26, 1
	v_cvt_f32_u32_e32 v236, v236
	v_sub_f32_e32 v236, 1.0, v236
	v_fmac_f32_e32 v94, s35, v236
	v_bfe_u32 v236, v235, 27, 1
	v_cvt_f32_u32_e32 v236, v236
	v_sub_f32_e32 v236, 1.0, v236
	v_fmac_f32_e32 v95, s35, v236
.Lovfnm_b00:
	v_max3_f32 v235, v80, v81, v82
	v_max3_f32 v235, v235, v83, v84
	v_max3_f32 v235, v235, v85, v86
	v_max3_f32 v235, v235, v87, v88
	v_max3_f32 v235, v235, v89, v90
	v_max3_f32 v235, v235, v91, v92
	v_max3_f32 v235, v235, v93, v94
	v_max_f32_e32 v235, v235, v95
	v_mov_b32_e32 v236, v235
	s_nop 1
	v_permlane32_swap_b32_e32 v235, v236
	v_max_f32_e32 v235, v235, v236
	v_max_f32_e32 v235, 0, v235
	v_exp_f32_e64 v237, -v235
	v_sub_f32_e32 v112, v112, v235
	v_sub_f32_e32 v113, v113, v235
	v_sub_f32_e32 v114, v114, v235
	v_sub_f32_e32 v115, v115, v235
	v_sub_f32_e32 v116, v116, v235
	v_sub_f32_e32 v117, v117, v235
	v_sub_f32_e32 v118, v118, v235
	v_sub_f32_e32 v119, v119, v235
	v_sub_f32_e32 v120, v120, v235
	v_sub_f32_e32 v121, v121, v235
	v_sub_f32_e32 v122, v122, v235
	v_sub_f32_e32 v123, v123, v235
	v_sub_f32_e32 v124, v124, v235
	v_sub_f32_e32 v125, v125, v235
	v_sub_f32_e32 v126, v126, v235
	v_sub_f32_e32 v127, v127, v235
	v_mul_f32_e32 v233, v233, v237
	v_mul_f32_e32 v32, v32, v237
	v_mul_f32_e32 v33, v33, v237
	v_mul_f32_e32 v34, v34, v237
	v_mul_f32_e32 v35, v35, v237
	v_mul_f32_e32 v36, v36, v237
	v_mul_f32_e32 v37, v37, v237
	v_mul_f32_e32 v38, v38, v237
	v_mul_f32_e32 v39, v39, v237
	v_mul_f32_e32 v40, v40, v237
	v_mul_f32_e32 v41, v41, v237
	v_mul_f32_e32 v42, v42, v237
	v_mul_f32_e32 v43, v43, v237
	v_mul_f32_e32 v44, v44, v237
	v_mul_f32_e32 v45, v45, v237
	v_mul_f32_e32 v46, v46, v237
	v_mul_f32_e32 v47, v47, v237
	v_mul_f32_e32 v48, v48, v237
	v_mul_f32_e32 v49, v49, v237
	v_mul_f32_e32 v50, v50, v237
	v_mul_f32_e32 v51, v51, v237
	v_mul_f32_e32 v52, v52, v237
	v_mul_f32_e32 v53, v53, v237
	v_mul_f32_e32 v54, v54, v237
	v_mul_f32_e32 v55, v55, v237
	v_mul_f32_e32 v56, v56, v237
	v_mul_f32_e32 v57, v57, v237
	v_mul_f32_e32 v58, v58, v237
	v_mul_f32_e32 v59, v59, v237
	v_mul_f32_e32 v60, v60, v237
	v_mul_f32_e32 v61, v61, v237
	v_mul_f32_e32 v62, v62, v237
	v_mul_f32_e32 v63, v63, v237
	v_sub_f32_e32 v80, v80, v235
	v_sub_f32_e32 v81, v81, v235
	v_sub_f32_e32 v82, v82, v235
	v_sub_f32_e32 v83, v83, v235
	v_sub_f32_e32 v84, v84, v235
	v_sub_f32_e32 v85, v85, v235
	v_sub_f32_e32 v86, v86, v235
	v_sub_f32_e32 v87, v87, v235
	v_sub_f32_e32 v88, v88, v235
	v_sub_f32_e32 v89, v89, v235
	v_sub_f32_e32 v90, v90, v235
	v_sub_f32_e32 v91, v91, v235
	v_sub_f32_e32 v92, v92, v235
	v_sub_f32_e32 v93, v93, v235
	v_sub_f32_e32 v94, v94, v235
	v_sub_f32_e32 v95, v95, v235
	v_exp_f32_e32 v80, v80
	v_exp_f32_e32 v81, v81
	v_exp_f32_e32 v82, v82
	v_exp_f32_e32 v83, v83
	v_exp_f32_e32 v84, v84
	v_exp_f32_e32 v85, v85
	v_exp_f32_e32 v86, v86
	v_exp_f32_e32 v87, v87
	v_exp_f32_e32 v88, v88
	v_exp_f32_e32 v89, v89
	v_exp_f32_e32 v90, v90
	v_exp_f32_e32 v91, v91
	v_exp_f32_e32 v92, v92
	v_exp_f32_e32 v93, v93
	v_exp_f32_e32 v94, v94
	v_exp_f32_e32 v95, v95
	s_nop 0
	v_add_f32_e32 v231, v80, v81
	v_add_f32_e32 v231, v231, v82
	v_add_f32_e32 v231, v231, v83
	v_add_f32_e32 v231, v231, v84
	v_add_f32_e32 v231, v231, v85
	v_add_f32_e32 v231, v231, v86
	v_add_f32_e32 v231, v231, v87
	v_add_f32_e32 v231, v231, v88
	v_add_f32_e32 v231, v231, v89
	v_add_f32_e32 v231, v231, v90
	v_add_f32_e32 v231, v231, v91
	v_add_f32_e32 v231, v231, v92
	v_add_f32_e32 v231, v231, v93
	v_add_f32_e32 v231, v231, v94
	v_add_f32_e32 v231, v231, v95
	v_cvt_pk_f16_f32 v168, v80, v81
	v_cvt_pk_f16_f32 v169, v82, v83
	v_cvt_pk_f16_f32 v170, v84, v85
	v_cvt_pk_f16_f32 v171, v86, v87
	v_cvt_pk_f16_f32 v172, v88, v89
	v_cvt_pk_f16_f32 v173, v90, v91
	v_cvt_pk_f16_f32 v174, v92, v93
	v_cvt_pk_f16_f32 v175, v94, v95
	s_branch .Lovfret_b00
.Lovf_a01:
	s_waitcnt lgkmcnt(0)
	s_nop 15
	s_nop 15
	s_nop 15
	ds_read_b128 v[168:171], v225 offset:4608
	ds_read_b128 v[172:175], v225 offset:4640
	s_waitcnt lgkmcnt(0)
	v_mfma_f32_32x32x16_f16 v[64:79], v[168:171], v[128:131], v[96:111]
	v_mfma_f32_32x32x16_f16 v[64:79], v[172:175], v[132:135], v[64:79]
	s_nop 15
	ds_read_b128 v[168:171], v225 offset:4672
	ds_read_b128 v[172:175], v225 offset:4704
	s_waitcnt lgkmcnt(0)
	v_mfma_f32_32x32x16_f16 v[64:79], v[168:171], v[136:139], v[64:79]
	v_mfma_f32_32x32x16_f16 v[64:79], v[172:175], v[140:143], v[64:79]
	s_nop 15
	s_nop 15
	s_cmp_eq_u64 s[20:21], -1
	s_cbranch_scc1 .Lovfnm_a01
	v_lshrrev_b32_e64 v235, v234, s21
	v_bfe_u32 v236, v235, 0, 1
	v_cvt_f32_u32_e32 v236, v236
	v_sub_f32_e32 v236, 1.0, v236
	v_fmac_f32_e32 v64, s35, v236
	v_bfe_u32 v236, v235, 1, 1
	v_cvt_f32_u32_e32 v236, v236
	v_sub_f32_e32 v236, 1.0, v236
	v_fmac_f32_e32 v65, s35, v236
	v_bfe_u32 v236, v235, 2, 1
	v_cvt_f32_u32_e32 v236, v236
	v_sub_f32_e32 v236, 1.0, v236
	v_fmac_f32_e32 v66, s35, v236
	v_bfe_u32 v236, v235, 3, 1
	v_cvt_f32_u32_e32 v236, v236
	v_sub_f32_e32 v236, 1.0, v236
	v_fmac_f32_e32 v67, s35, v236
	v_bfe_u32 v236, v235, 8, 1
	v_cvt_f32_u32_e32 v236, v236
	v_sub_f32_e32 v236, 1.0, v236
	v_fmac_f32_e32 v68, s35, v236
	v_bfe_u32 v236, v235, 9, 1
	v_cvt_f32_u32_e32 v236, v236
	v_sub_f32_e32 v236, 1.0, v236
	v_fmac_f32_e32 v69, s35, v236
	v_bfe_u32 v236, v235, 10, 1
	v_cvt_f32_u32_e32 v236, v236
	v_sub_f32_e32 v236, 1.0, v236
	v_fmac_f32_e32 v70, s35, v236
	v_bfe_u32 v236, v235, 11, 1
	v_cvt_f32_u32_e32 v236, v236
	v_sub_f32_e32 v236, 1.0, v236
	v_fmac_f32_e32 v71, s35, v236
	v_bfe_u32 v236, v235, 16, 1
	v_cvt_f32_u32_e32 v236, v236
	v_sub_f32_e32 v236, 1.0, v236
	v_fmac_f32_e32 v72, s35, v236
	v_bfe_u32 v236, v235, 17, 1
	v_cvt_f32_u32_e32 v236, v236
	v_sub_f32_e32 v236, 1.0, v236
	v_fmac_f32_e32 v73, s35, v236
	v_bfe_u32 v236, v235, 18, 1
	v_cvt_f32_u32_e32 v236, v236
	v_sub_f32_e32 v236, 1.0, v236
	v_fmac_f32_e32 v74, s35, v236
	v_bfe_u32 v236, v235, 19, 1
	v_cvt_f32_u32_e32 v236, v236
	v_sub_f32_e32 v236, 1.0, v236
	v_fmac_f32_e32 v75, s35, v236
	v_bfe_u32 v236, v235, 24, 1
	v_cvt_f32_u32_e32 v236, v236
	v_sub_f32_e32 v236, 1.0, v236
	v_fmac_f32_e32 v76, s35, v236
	v_bfe_u32 v236, v235, 25, 1
	v_cvt_f32_u32_e32 v236, v236
	v_sub_f32_e32 v236, 1.0, v236
	v_fmac_f32_e32 v77, s35, v236
	v_bfe_u32 v236, v235, 26, 1
	v_cvt_f32_u32_e32 v236, v236
	v_sub_f32_e32 v236, 1.0, v236
	v_fmac_f32_e32 v78, s35, v236
	v_bfe_u32 v236, v235, 27, 1
	v_cvt_f32_u32_e32 v236, v236
	v_sub_f32_e32 v236, 1.0, v236
	v_fmac_f32_e32 v79, s35, v236

.Lovf_b01:
	s_waitcnt lgkmcnt(0)
	s_nop 15
	s_nop 15
	s_nop 15
	ds_read_b128 v[160:163], v225 offset:4608
	ds_read_b128 v[164:167], v225 offset:4640
	s_waitcnt lgkmcnt(0)
	v_mfma_f32_32x32x16_f16 v[80:95], v[160:163], v[144:147], v[112:127]
	v_mfma_f32_32x32x16_f16 v[80:95], v[164:167], v[148:151], v[80:95]
	s_nop 15
	ds_read_b128 v[160:163], v225 offset:4672
	ds_read_b128 v[164:167], v225 offset:4704
	s_waitcnt lgkmcnt(0)
	v_mfma_f32_32x32x16_f16 v[80:95], v[160:163], v[152:155], v[80:95]
	v_mfma_f32_32x32x16_f16 v[80:95], v[164:167], v[156:159], v[80:95]
	s_nop 15
	s_nop 15
	s_cmp_eq_u64 s[20:21], -1
	s_cbranch_scc1 .Lovfnm_b01
	v_lshrrev_b32_e64 v235, v234, s21
	v_bfe_u32 v236, v235, 0, 1
	v_cvt_f32_u32_e32 v236, v236
	v_sub_f32_e32 v236, 1.0, v236
	v_fmac_f32_e32 v80, s35, v236
	v_bfe_u32 v236, v235, 1, 1
	v_cvt_f32_u32_e32 v236, v236
	v_sub_f32_e32 v236, 1.0, v236
	v_fmac_f32_e32 v81, s35, v236
	v_bfe_u32 v236, v235, 2, 1
	v_cvt_f32_u32_e32 v236, v236
	v_sub_f32_e32 v236, 1.0, v236
	v_fmac_f32_e32 v82, s35, v236
	v_bfe_u32 v236, v235, 3, 1
	v_cvt_f32_u32_e32 v236, v236
	v_sub_f32_e32 v236, 1.0, v236
	v_fmac_f32_e32 v83, s35, v236
	v_bfe_u32 v236, v235, 8, 1
	v_cvt_f32_u32_e32 v236, v236
	v_sub_f32_e32 v236, 1.0, v236
	v_fmac_f32_e32 v84, s35, v236
	v_bfe_u32 v236, v235, 9, 1
	v_cvt_f32_u32_e32 v236, v236
	v_sub_f32_e32 v236, 1.0, v236
	v_fmac_f32_e32 v85, s35, v236
	v_bfe_u32 v236, v235, 10, 1
	v_cvt_f32_u32_e32 v236, v236
	v_sub_f32_e32 v236, 1.0, v236
	v_fmac_f32_e32 v86, s35, v236
	v_bfe_u32 v236, v235, 11, 1
	v_cvt_f32_u32_e32 v236, v236
	v_sub_f32_e32 v236, 1.0, v236
	v_fmac_f32_e32 v87, s35, v236
	v_bfe_u32 v236, v235, 16, 1
	v_cvt_f32_u32_e32 v236, v236
	v_sub_f32_e32 v236, 1.0, v236
	v_fmac_f32_e32 v88, s35, v236
	v_bfe_u32 v236, v235, 17, 1
	v_cvt_f32_u32_e32 v236, v236
	v_sub_f32_e32 v236, 1.0, v236
	v_fmac_f32_e32 v89, s35, v236
	v_bfe_u32 v236, v235, 18, 1
	v_cvt_f32_u32_e32 v236, v236
	v_sub_f32_e32 v236, 1.0, v236
	v_fmac_f32_e32 v90, s35, v236
	v_bfe_u32 v236, v235, 19, 1
	v_cvt_f32_u32_e32 v236, v236
	v_sub_f32_e32 v236, 1.0, v236
	v_fmac_f32_e32 v91, s35, v236
	v_bfe_u32 v236, v235, 24, 1
	v_cvt_f32_u32_e32 v236, v236
	v_sub_f32_e32 v236, 1.0, v236
	v_fmac_f32_e32 v92, s35, v236
	v_bfe_u32 v236, v235, 25, 1
	v_cvt_f32_u32_e32 v236, v236
	v_sub_f32_e32 v236, 1.0, v236
	v_fmac_f32_e32 v93, s35, v236
	v_bfe_u32 v236, v235, 26, 1
	v_cvt_f32_u32_e32 v236, v236
	v_sub_f32_e32 v236, 1.0, v236
	v_fmac_f32_e32 v94, s35, v236
	v_bfe_u32 v236, v235, 27, 1
	v_cvt_f32_u32_e32 v236, v236
	v_sub_f32_e32 v236, 1.0, v236
	v_fmac_f32_e32 v95, s35, v236

.Lovf_a10:
	s_waitcnt lgkmcnt(0)
	s_nop 15
	s_nop 15
	s_nop 15
	ds_read_b128 v[168:171], v225 offset:9216
	ds_read_b128 v[172:175], v225 offset:9248
	s_waitcnt lgkmcnt(0)
	v_mfma_f32_32x32x16_f16 v[64:79], v[168:171], v[128:131], v[96:111]
	v_mfma_f32_32x32x16_f16 v[64:79], v[172:175], v[132:135], v[64:79]
	s_nop 15
	ds_read_b128 v[168:171], v225 offset:9280
	ds_read_b128 v[172:175], v225 offset:9312
	s_waitcnt lgkmcnt(0)
	v_mfma_f32_32x32x16_f16 v[64:79], v[168:171], v[136:139], v[64:79]
	v_mfma_f32_32x32x16_f16 v[64:79], v[172:175], v[140:143], v[64:79]
	s_nop 15
	s_nop 15
	s_cmp_eq_u64 s[20:21], -1
	s_cbranch_scc1 .Lovfnm_a10
	v_lshrrev_b32_e64 v235, v234, s20
	v_bfe_u32 v236, v235, 0, 1
	v_cvt_f32_u32_e32 v236, v236
	v_sub_f32_e32 v236, 1.0, v236
	v_fmac_f32_e32 v64, s35, v236
	v_bfe_u32 v236, v235, 1, 1
	v_cvt_f32_u32_e32 v236, v236
	v_sub_f32_e32 v236, 1.0, v236
	v_fmac_f32_e32 v65, s35, v236
	v_bfe_u32 v236, v235, 2, 1
	v_cvt_f32_u32_e32 v236, v236
	v_sub_f32_e32 v236, 1.0, v236
	v_fmac_f32_e32 v66, s35, v236
	v_bfe_u32 v236, v235, 3, 1
	v_cvt_f32_u32_e32 v236, v236
	v_sub_f32_e32 v236, 1.0, v236
	v_fmac_f32_e32 v67, s35, v236
	v_bfe_u32 v236, v235, 8, 1
	v_cvt_f32_u32_e32 v236, v236
	v_sub_f32_e32 v236, 1.0, v236
	v_fmac_f32_e32 v68, s35, v236
	v_bfe_u32 v236, v235, 9, 1
	v_cvt_f32_u32_e32 v236, v236
	v_sub_f32_e32 v236, 1.0, v236
	v_fmac_f32_e32 v69, s35, v236
	v_bfe_u32 v236, v235, 10, 1
	v_cvt_f32_u32_e32 v236, v236
	v_sub_f32_e32 v236, 1.0, v236
	v_fmac_f32_e32 v70, s35, v236
	v_bfe_u32 v236, v235, 11, 1
	v_cvt_f32_u32_e32 v236, v236
	v_sub_f32_e32 v236, 1.0, v236
	v_fmac_f32_e32 v71, s35, v236
	v_bfe_u32 v236, v235, 16, 1
	v_cvt_f32_u32_e32 v236, v236
	v_sub_f32_e32 v236, 1.0, v236
	v_fmac_f32_e32 v72, s35, v236
	v_bfe_u32 v236, v235, 17, 1
	v_cvt_f32_u32_e32 v236, v236
	v_sub_f32_e32 v236, 1.0, v236
	v_fmac_f32_e32 v73, s35, v236
	v_bfe_u32 v236, v235, 18, 1
	v_cvt_f32_u32_e32 v236, v236
	v_sub_f32_e32 v236, 1.0, v236
	v_fmac_f32_e32 v74, s35, v236
	v_bfe_u32 v236, v235, 19, 1
	v_cvt_f32_u32_e32 v236, v236
	v_sub_f32_e32 v236, 1.0, v236
	v_fmac_f32_e32 v75, s35, v236
	v_bfe_u32 v236, v235, 24, 1
	v_cvt_f32_u32_e32 v236, v236
	v_sub_f32_e32 v236, 1.0, v236
	v_fmac_f32_e32 v76, s35, v236
	v_bfe_u32 v236, v235, 25, 1
	v_cvt_f32_u32_e32 v236, v236
	v_sub_f32_e32 v236, 1.0, v236
	v_fmac_f32_e32 v77, s35, v236
	v_bfe_u32 v236, v235, 26, 1
	v_cvt_f32_u32_e32 v236, v236
	v_sub_f32_e32 v236, 1.0, v236
	v_fmac_f32_e32 v78, s35, v236
	v_bfe_u32 v236, v235, 27, 1
	v_cvt_f32_u32_e32 v236, v236
	v_sub_f32_e32 v236, 1.0, v236
	v_fmac_f32_e32 v79, s35, v236

.Lovf_b10:
	s_waitcnt lgkmcnt(0)
	s_nop 15
	s_nop 15
	s_nop 15
	ds_read_b128 v[160:163], v225 offset:9216
	ds_read_b128 v[164:167], v225 offset:9248
	s_waitcnt lgkmcnt(0)
	v_mfma_f32_32x32x16_f16 v[80:95], v[160:163], v[144:147], v[112:127]
	v_mfma_f32_32x32x16_f16 v[80:95], v[164:167], v[148:151], v[80:95]
	s_nop 15
	ds_read_b128 v[160:163], v225 offset:9280
	ds_read_b128 v[164:167], v225 offset:9312
	s_waitcnt lgkmcnt(0)
	v_mfma_f32_32x32x16_f16 v[80:95], v[160:163], v[152:155], v[80:95]
	v_mfma_f32_32x32x16_f16 v[80:95], v[164:167], v[156:159], v[80:95]
	s_nop 15
	s_nop 15
	s_cmp_eq_u64 s[20:21], -1
	s_cbranch_scc1 .Lovfnm_b10
	v_lshrrev_b32_e64 v235, v234, s20
	v_bfe_u32 v236, v235, 0, 1
	v_cvt_f32_u32_e32 v236, v236
	v_sub_f32_e32 v236, 1.0, v236
	v_fmac_f32_e32 v80, s35, v236
	v_bfe_u32 v236, v235, 1, 1
	v_cvt_f32_u32_e32 v236, v236
	v_sub_f32_e32 v236, 1.0, v236
	v_fmac_f32_e32 v81, s35, v236
	v_bfe_u32 v236, v235, 2, 1
	v_cvt_f32_u32_e32 v236, v236
	v_sub_f32_e32 v236, 1.0, v236
	v_fmac_f32_e32 v82, s35, v236
	v_bfe_u32 v236, v235, 3, 1
	v_cvt_f32_u32_e32 v236, v236
	v_sub_f32_e32 v236, 1.0, v236
	v_fmac_f32_e32 v83, s35, v236
	v_bfe_u32 v236, v235, 8, 1
	v_cvt_f32_u32_e32 v236, v236
	v_sub_f32_e32 v236, 1.0, v236
	v_fmac_f32_e32 v84, s35, v236
	v_bfe_u32 v236, v235, 9, 1
	v_cvt_f32_u32_e32 v236, v236
	v_sub_f32_e32 v236, 1.0, v236
	v_fmac_f32_e32 v85, s35, v236
	v_bfe_u32 v236, v235, 10, 1
	v_cvt_f32_u32_e32 v236, v236
	v_sub_f32_e32 v236, 1.0, v236
	v_fmac_f32_e32 v86, s35, v236
	v_bfe_u32 v236, v235, 11, 1
	v_cvt_f32_u32_e32 v236, v236
	v_sub_f32_e32 v236, 1.0, v236
	v_fmac_f32_e32 v87, s35, v236
	v_bfe_u32 v236, v235, 16, 1
	v_cvt_f32_u32_e32 v236, v236
	v_sub_f32_e32 v236, 1.0, v236
	v_fmac_f32_e32 v88, s35, v236
	v_bfe_u32 v236, v235, 17, 1
	v_cvt_f32_u32_e32 v236, v236
	v_sub_f32_e32 v236, 1.0, v236
	v_fmac_f32_e32 v89, s35, v236
	v_bfe_u32 v236, v235, 18, 1
	v_cvt_f32_u32_e32 v236, v236
	v_sub_f32_e32 v236, 1.0, v236
	v_fmac_f32_e32 v90, s35, v236
	v_bfe_u32 v236, v235, 19, 1
	v_cvt_f32_u32_e32 v236, v236
	v_sub_f32_e32 v236, 1.0, v236
	v_fmac_f32_e32 v91, s35, v236
	v_bfe_u32 v236, v235, 24, 1
	v_cvt_f32_u32_e32 v236, v236
	v_sub_f32_e32 v236, 1.0, v236
	v_fmac_f32_e32 v92, s35, v236
	v_bfe_u32 v236, v235, 25, 1
	v_cvt_f32_u32_e32 v236, v236
	v_sub_f32_e32 v236, 1.0, v236
	v_fmac_f32_e32 v93, s35, v236
	v_bfe_u32 v236, v235, 26, 1
	v_cvt_f32_u32_e32 v236, v236
	v_sub_f32_e32 v236, 1.0, v236
	v_fmac_f32_e32 v94, s35, v236
	v_bfe_u32 v236, v235, 27, 1
	v_cvt_f32_u32_e32 v236, v236
	v_sub_f32_e32 v236, 1.0, v236
	v_fmac_f32_e32 v95, s35, v236

.Lovf_a11:
	s_waitcnt lgkmcnt(0)
	s_nop 15
	s_nop 15
	s_nop 15
	ds_read_b128 v[168:171], v225 offset:13824
	ds_read_b128 v[172:175], v225 offset:13856
	s_waitcnt lgkmcnt(0)
	v_mfma_f32_32x32x16_f16 v[64:79], v[168:171], v[128:131], v[96:111]
	v_mfma_f32_32x32x16_f16 v[64:79], v[172:175], v[132:135], v[64:79]
	s_nop 15
	ds_read_b128 v[168:171], v225 offset:13888
	ds_read_b128 v[172:175], v225 offset:13920
	s_waitcnt lgkmcnt(0)
	v_mfma_f32_32x32x16_f16 v[64:79], v[168:171], v[136:139], v[64:79]
	v_mfma_f32_32x32x16_f16 v[64:79], v[172:175], v[140:143], v[64:79]
	s_nop 15
	s_nop 15
	s_cmp_eq_u64 s[20:21], -1
	s_cbranch_scc1 .Lovfnm_a11
	v_lshrrev_b32_e64 v235, v234, s21
	v_bfe_u32 v236, v235, 0, 1
	v_cvt_f32_u32_e32 v236, v236
	v_sub_f32_e32 v236, 1.0, v236
	v_fmac_f32_e32 v64, s35, v236
	v_bfe_u32 v236, v235, 1, 1
	v_cvt_f32_u32_e32 v236, v236
	v_sub_f32_e32 v236, 1.0, v236
	v_fmac_f32_e32 v65, s35, v236
	v_bfe_u32 v236, v235, 2, 1
	v_cvt_f32_u32_e32 v236, v236
	v_sub_f32_e32 v236, 1.0, v236
	v_fmac_f32_e32 v66, s35, v236
	v_bfe_u32 v236, v235, 3, 1
	v_cvt_f32_u32_e32 v236, v236
	v_sub_f32_e32 v236, 1.0, v236
	v_fmac_f32_e32 v67, s35, v236
	v_bfe_u32 v236, v235, 8, 1
	v_cvt_f32_u32_e32 v236, v236
	v_sub_f32_e32 v236, 1.0, v236
	v_fmac_f32_e32 v68, s35, v236
	v_bfe_u32 v236, v235, 9, 1
	v_cvt_f32_u32_e32 v236, v236
	v_sub_f32_e32 v236, 1.0, v236
	v_fmac_f32_e32 v69, s35, v236
	v_bfe_u32 v236, v235, 10, 1
	v_cvt_f32_u32_e32 v236, v236
	v_sub_f32_e32 v236, 1.0, v236
	v_fmac_f32_e32 v70, s35, v236
	v_bfe_u32 v236, v235, 11, 1
	v_cvt_f32_u32_e32 v236, v236
	v_sub_f32_e32 v236, 1.0, v236
	v_fmac_f32_e32 v71, s35, v236
	v_bfe_u32 v236, v235, 16, 1
	v_cvt_f32_u32_e32 v236, v236
	v_sub_f32_e32 v236, 1.0, v236
	v_fmac_f32_e32 v72, s35, v236
	v_bfe_u32 v236, v235, 17, 1
	v_cvt_f32_u32_e32 v236, v236
	v_sub_f32_e32 v236, 1.0, v236
	v_fmac_f32_e32 v73, s35, v236
	v_bfe_u32 v236, v235, 18, 1
	v_cvt_f32_u32_e32 v236, v236
	v_sub_f32_e32 v236, 1.0, v236
	v_fmac_f32_e32 v74, s35, v236
	v_bfe_u32 v236, v235, 19, 1
	v_cvt_f32_u32_e32 v236, v236
	v_sub_f32_e32 v236, 1.0, v236
	v_fmac_f32_e32 v75, s35, v236
	v_bfe_u32 v236, v235, 24, 1
	v_cvt_f32_u32_e32 v236, v236
	v_sub_f32_e32 v236, 1.0, v236
	v_fmac_f32_e32 v76, s35, v236
	v_bfe_u32 v236, v235, 25, 1
	v_cvt_f32_u32_e32 v236, v236
	v_sub_f32_e32 v236, 1.0, v236
	v_fmac_f32_e32 v77, s35, v236
	v_bfe_u32 v236, v235, 26, 1
	v_cvt_f32_u32_e32 v236, v236
	v_sub_f32_e32 v236, 1.0, v236
	v_fmac_f32_e32 v78, s35, v236
	v_bfe_u32 v236, v235, 27, 1
	v_cvt_f32_u32_e32 v236, v236
	v_sub_f32_e32 v236, 1.0, v236
	v_fmac_f32_e32 v79, s35, v236

.Lovf_b11:
	s_waitcnt lgkmcnt(0)
	s_nop 15
	s_nop 15
	s_nop 15
	ds_read_b128 v[160:163], v225 offset:13824
	ds_read_b128 v[164:167], v225 offset:13856
	s_waitcnt lgkmcnt(0)
	v_mfma_f32_32x32x16_f16 v[80:95], v[160:163], v[144:147], v[112:127]
	v_mfma_f32_32x32x16_f16 v[80:95], v[164:167], v[148:151], v[80:95]
	s_nop 15
	ds_read_b128 v[160:163], v225 offset:13888
	ds_read_b128 v[164:167], v225 offset:13920
	s_waitcnt lgkmcnt(0)
	v_mfma_f32_32x32x16_f16 v[80:95], v[160:163], v[152:155], v[80:95]
	v_mfma_f32_32x32x16_f16 v[80:95], v[164:167], v[156:159], v[80:95]
	s_nop 15
	s_nop 15
	s_cmp_eq_u64 s[20:21], -1
	s_cbranch_scc1 .Lovfnm_b11
	v_lshrrev_b32_e64 v235, v234, s21
	v_bfe_u32 v236, v235, 0, 1
	v_cvt_f32_u32_e32 v236, v236
	v_sub_f32_e32 v236, 1.0, v236
	v_fmac_f32_e32 v80, s35, v236
	v_bfe_u32 v236, v235, 1, 1
	v_cvt_f32_u32_e32 v236, v236
	v_sub_f32_e32 v236, 1.0, v236
	v_fmac_f32_e32 v81, s35, v236
	v_bfe_u32 v236, v235, 2, 1
	v_cvt_f32_u32_e32 v236, v236
	v_sub_f32_e32 v236, 1.0, v236
	v_fmac_f32_e32 v82, s35, v236
	v_bfe_u32 v236, v235, 3, 1
	v_cvt_f32_u32_e32 v236, v236
	v_sub_f32_e32 v236, 1.0, v236
	v_fmac_f32_e32 v83, s35, v236
	v_bfe_u32 v236, v235, 8, 1
	v_cvt_f32_u32_e32 v236, v236
	v_sub_f32_e32 v236, 1.0, v236
	v_fmac_f32_e32 v84, s35, v236
	v_bfe_u32 v236, v235, 9, 1
	v_cvt_f32_u32_e32 v236, v236
	v_sub_f32_e32 v236, 1.0, v236
	v_fmac_f32_e32 v85, s35, v236
	v_bfe_u32 v236, v235, 10, 1
	v_cvt_f32_u32_e32 v236, v236
	v_sub_f32_e32 v236, 1.0, v236
	v_fmac_f32_e32 v86, s35, v236
	v_bfe_u32 v236, v235, 11, 1
	v_cvt_f32_u32_e32 v236, v236
	v_sub_f32_e32 v236, 1.0, v236
	v_fmac_f32_e32 v87, s35, v236
	v_bfe_u32 v236, v235, 16, 1
	v_cvt_f32_u32_e32 v236, v236
	v_sub_f32_e32 v236, 1.0, v236
	v_fmac_f32_e32 v88, s35, v236
	v_bfe_u32 v236, v235, 17, 1
	v_cvt_f32_u32_e32 v236, v236
	v_sub_f32_e32 v236, 1.0, v236
	v_fmac_f32_e32 v89, s35, v236
	v_bfe_u32 v236, v235, 18, 1
	v_cvt_f32_u32_e32 v236, v236
	v_sub_f32_e32 v236, 1.0, v236
	v_fmac_f32_e32 v90, s35, v236
	v_bfe_u32 v236, v235, 19, 1
	v_cvt_f32_u32_e32 v236, v236
	v_sub_f32_e32 v236, 1.0, v236
	v_fmac_f32_e32 v91, s35, v236
	v_bfe_u32 v236, v235, 24, 1
	v_cvt_f32_u32_e32 v236, v236
	v_sub_f32_e32 v236, 1.0, v236
	v_fmac_f32_e32 v92, s35, v236
	v_bfe_u32 v236, v235, 25, 1
	v_cvt_f32_u32_e32 v236, v236
	v_sub_f32_e32 v236, 1.0, v236
	v_fmac_f32_e32 v93, s35, v236
	v_bfe_u32 v236, v235, 26, 1
	v_cvt_f32_u32_e32 v236, v236
	v_sub_f32_e32 v236, 1.0, v236
	v_fmac_f32_e32 v94, s35, v236
	v_bfe_u32 v236, v235, 27, 1
	v_cvt_f32_u32_e32 v236, v236
	v_sub_f32_e32 v236, 1.0, v236
	v_fmac_f32_e32 v95, s35, v236

.Lovf_a20:
	s_waitcnt lgkmcnt(0)
	s_nop 15
	s_nop 15
	s_nop 15
	ds_read_b128 v[168:171], v225 offset:18432
	ds_read_b128 v[172:175], v225 offset:18464
	s_waitcnt lgkmcnt(0)
	v_mfma_f32_32x32x16_f16 v[64:79], v[168:171], v[128:131], v[96:111]
	v_mfma_f32_32x32x16_f16 v[64:79], v[172:175], v[132:135], v[64:79]
	s_nop 15
	ds_read_b128 v[168:171], v225 offset:18496
	ds_read_b128 v[172:175], v225 offset:18528
	s_waitcnt lgkmcnt(0)
	v_mfma_f32_32x32x16_f16 v[64:79], v[168:171], v[136:139], v[64:79]
	v_mfma_f32_32x32x16_f16 v[64:79], v[172:175], v[140:143], v[64:79]
	s_nop 15
	s_nop 15
	s_cmp_eq_u64 s[20:21], -1
	s_cbranch_scc1 .Lovfnm_a20
	v_lshrrev_b32_e64 v235, v234, s20
	v_bfe_u32 v236, v235, 0, 1
	v_cvt_f32_u32_e32 v236, v236
	v_sub_f32_e32 v236, 1.0, v236
	v_fmac_f32_e32 v64, s35, v236
	v_bfe_u32 v236, v235, 1, 1
	v_cvt_f32_u32_e32 v236, v236
	v_sub_f32_e32 v236, 1.0, v236
	v_fmac_f32_e32 v65, s35, v236
	v_bfe_u32 v236, v235, 2, 1
	v_cvt_f32_u32_e32 v236, v236
	v_sub_f32_e32 v236, 1.0, v236
	v_fmac_f32_e32 v66, s35, v236
	v_bfe_u32 v236, v235, 3, 1
	v_cvt_f32_u32_e32 v236, v236
	v_sub_f32_e32 v236, 1.0, v236
	v_fmac_f32_e32 v67, s35, v236
	v_bfe_u32 v236, v235, 8, 1
	v_cvt_f32_u32_e32 v236, v236
	v_sub_f32_e32 v236, 1.0, v236
	v_fmac_f32_e32 v68, s35, v236
	v_bfe_u32 v236, v235, 9, 1
	v_cvt_f32_u32_e32 v236, v236
	v_sub_f32_e32 v236, 1.0, v236
	v_fmac_f32_e32 v69, s35, v236
	v_bfe_u32 v236, v235, 10, 1
	v_cvt_f32_u32_e32 v236, v236
	v_sub_f32_e32 v236, 1.0, v236
	v_fmac_f32_e32 v70, s35, v236
	v_bfe_u32 v236, v235, 11, 1
	v_cvt_f32_u32_e32 v236, v236
	v_sub_f32_e32 v236, 1.0, v236
	v_fmac_f32_e32 v71, s35, v236
	v_bfe_u32 v236, v235, 16, 1
	v_cvt_f32_u32_e32 v236, v236
	v_sub_f32_e32 v236, 1.0, v236
	v_fmac_f32_e32 v72, s35, v236
	v_bfe_u32 v236, v235, 17, 1
	v_cvt_f32_u32_e32 v236, v236
	v_sub_f32_e32 v236, 1.0, v236
	v_fmac_f32_e32 v73, s35, v236
	v_bfe_u32 v236, v235, 18, 1
	v_cvt_f32_u32_e32 v236, v236
	v_sub_f32_e32 v236, 1.0, v236
	v_fmac_f32_e32 v74, s35, v236
	v_bfe_u32 v236, v235, 19, 1
	v_cvt_f32_u32_e32 v236, v236
	v_sub_f32_e32 v236, 1.0, v236
	v_fmac_f32_e32 v75, s35, v236
	v_bfe_u32 v236, v235, 24, 1
	v_cvt_f32_u32_e32 v236, v236
	v_sub_f32_e32 v236, 1.0, v236
	v_fmac_f32_e32 v76, s35, v236
	v_bfe_u32 v236, v235, 25, 1
	v_cvt_f32_u32_e32 v236, v236
	v_sub_f32_e32 v236, 1.0, v236
	v_fmac_f32_e32 v77, s35, v236
	v_bfe_u32 v236, v235, 26, 1
	v_cvt_f32_u32_e32 v236, v236
	v_sub_f32_e32 v236, 1.0, v236
	v_fmac_f32_e32 v78, s35, v236
	v_bfe_u32 v236, v235, 27, 1
	v_cvt_f32_u32_e32 v236, v236
	v_sub_f32_e32 v236, 1.0, v236
	v_fmac_f32_e32 v79, s35, v236

.Lovf_b20:
	s_waitcnt lgkmcnt(0)
	s_nop 15
	s_nop 15
	s_nop 15
	ds_read_b128 v[160:163], v225 offset:18432
	ds_read_b128 v[164:167], v225 offset:18464
	s_waitcnt lgkmcnt(0)
	v_mfma_f32_32x32x16_f16 v[80:95], v[160:163], v[144:147], v[112:127]
	v_mfma_f32_32x32x16_f16 v[80:95], v[164:167], v[148:151], v[80:95]
	s_nop 15
	ds_read_b128 v[160:163], v225 offset:18496
	ds_read_b128 v[164:167], v225 offset:18528
	s_waitcnt lgkmcnt(0)
	v_mfma_f32_32x32x16_f16 v[80:95], v[160:163], v[152:155], v[80:95]
	v_mfma_f32_32x32x16_f16 v[80:95], v[164:167], v[156:159], v[80:95]
	s_nop 15
	s_nop 15
	s_cmp_eq_u64 s[20:21], -1
	s_cbranch_scc1 .Lovfnm_b20
	v_lshrrev_b32_e64 v235, v234, s20
	v_bfe_u32 v236, v235, 0, 1
	v_cvt_f32_u32_e32 v236, v236
	v_sub_f32_e32 v236, 1.0, v236
	v_fmac_f32_e32 v80, s35, v236
	v_bfe_u32 v236, v235, 1, 1
	v_cvt_f32_u32_e32 v236, v236
	v_sub_f32_e32 v236, 1.0, v236
	v_fmac_f32_e32 v81, s35, v236
	v_bfe_u32 v236, v235, 2, 1
	v_cvt_f32_u32_e32 v236, v236
	v_sub_f32_e32 v236, 1.0, v236
	v_fmac_f32_e32 v82, s35, v236
	v_bfe_u32 v236, v235, 3, 1
	v_cvt_f32_u32_e32 v236, v236
	v_sub_f32_e32 v236, 1.0, v236
	v_fmac_f32_e32 v83, s35, v236
	v_bfe_u32 v236, v235, 8, 1
	v_cvt_f32_u32_e32 v236, v236
	v_sub_f32_e32 v236, 1.0, v236
	v_fmac_f32_e32 v84, s35, v236
	v_bfe_u32 v236, v235, 9, 1
	v_cvt_f32_u32_e32 v236, v236
	v_sub_f32_e32 v236, 1.0, v236
	v_fmac_f32_e32 v85, s35, v236
	v_bfe_u32 v236, v235, 10, 1
	v_cvt_f32_u32_e32 v236, v236
	v_sub_f32_e32 v236, 1.0, v236
	v_fmac_f32_e32 v86, s35, v236
	v_bfe_u32 v236, v235, 11, 1
	v_cvt_f32_u32_e32 v236, v236
	v_sub_f32_e32 v236, 1.0, v236
	v_fmac_f32_e32 v87, s35, v236
	v_bfe_u32 v236, v235, 16, 1
	v_cvt_f32_u32_e32 v236, v236
	v_sub_f32_e32 v236, 1.0, v236
	v_fmac_f32_e32 v88, s35, v236
	v_bfe_u32 v236, v235, 17, 1
	v_cvt_f32_u32_e32 v236, v236
	v_sub_f32_e32 v236, 1.0, v236
	v_fmac_f32_e32 v89, s35, v236
	v_bfe_u32 v236, v235, 18, 1
	v_cvt_f32_u32_e32 v236, v236
	v_sub_f32_e32 v236, 1.0, v236
	v_fmac_f32_e32 v90, s35, v236
	v_bfe_u32 v236, v235, 19, 1
	v_cvt_f32_u32_e32 v236, v236
	v_sub_f32_e32 v236, 1.0, v236
	v_fmac_f32_e32 v91, s35, v236
	v_bfe_u32 v236, v235, 24, 1
	v_cvt_f32_u32_e32 v236, v236
	v_sub_f32_e32 v236, 1.0, v236
	v_fmac_f32_e32 v92, s35, v236
	v_bfe_u32 v236, v235, 25, 1
	v_cvt_f32_u32_e32 v236, v236
	v_sub_f32_e32 v236, 1.0, v236
	v_fmac_f32_e32 v93, s35, v236
	v_bfe_u32 v236, v235, 26, 1
	v_cvt_f32_u32_e32 v236, v236
	v_sub_f32_e32 v236, 1.0, v236
	v_fmac_f32_e32 v94, s35, v236
	v_bfe_u32 v236, v235, 27, 1
	v_cvt_f32_u32_e32 v236, v236
	v_sub_f32_e32 v236, 1.0, v236
	v_fmac_f32_e32 v95, s35, v236

.Lovf_a21:
	s_waitcnt lgkmcnt(0)
	s_nop 15
	s_nop 15
	s_nop 15
	ds_read_b128 v[168:171], v225 offset:23040
	ds_read_b128 v[172:175], v225 offset:23072
	s_waitcnt lgkmcnt(0)
	v_mfma_f32_32x32x16_f16 v[64:79], v[168:171], v[128:131], v[96:111]
	v_mfma_f32_32x32x16_f16 v[64:79], v[172:175], v[132:135], v[64:79]
	s_nop 15
	ds_read_b128 v[168:171], v225 offset:23104
	ds_read_b128 v[172:175], v225 offset:23136
	s_waitcnt lgkmcnt(0)
	v_mfma_f32_32x32x16_f16 v[64:79], v[168:171], v[136:139], v[64:79]
	v_mfma_f32_32x32x16_f16 v[64:79], v[172:175], v[140:143], v[64:79]
	s_nop 15
	s_nop 15
	s_cmp_eq_u64 s[20:21], -1
	s_cbranch_scc1 .Lovfnm_a21
	v_lshrrev_b32_e64 v235, v234, s21
	v_bfe_u32 v236, v235, 0, 1
	v_cvt_f32_u32_e32 v236, v236
	v_sub_f32_e32 v236, 1.0, v236
	v_fmac_f32_e32 v64, s35, v236
	v_bfe_u32 v236, v235, 1, 1
	v_cvt_f32_u32_e32 v236, v236
	v_sub_f32_e32 v236, 1.0, v236
	v_fmac_f32_e32 v65, s35, v236
	v_bfe_u32 v236, v235, 2, 1
	v_cvt_f32_u32_e32 v236, v236
	v_sub_f32_e32 v236, 1.0, v236
	v_fmac_f32_e32 v66, s35, v236
	v_bfe_u32 v236, v235, 3, 1
	v_cvt_f32_u32_e32 v236, v236
	v_sub_f32_e32 v236, 1.0, v236
	v_fmac_f32_e32 v67, s35, v236
	v_bfe_u32 v236, v235, 8, 1
	v_cvt_f32_u32_e32 v236, v236
	v_sub_f32_e32 v236, 1.0, v236
	v_fmac_f32_e32 v68, s35, v236
	v_bfe_u32 v236, v235, 9, 1
	v_cvt_f32_u32_e32 v236, v236
	v_sub_f32_e32 v236, 1.0, v236
	v_fmac_f32_e32 v69, s35, v236
	v_bfe_u32 v236, v235, 10, 1
	v_cvt_f32_u32_e32 v236, v236
	v_sub_f32_e32 v236, 1.0, v236
	v_fmac_f32_e32 v70, s35, v236
	v_bfe_u32 v236, v235, 11, 1
	v_cvt_f32_u32_e32 v236, v236
	v_sub_f32_e32 v236, 1.0, v236
	v_fmac_f32_e32 v71, s35, v236
	v_bfe_u32 v236, v235, 16, 1
	v_cvt_f32_u32_e32 v236, v236
	v_sub_f32_e32 v236, 1.0, v236
	v_fmac_f32_e32 v72, s35, v236
	v_bfe_u32 v236, v235, 17, 1
	v_cvt_f32_u32_e32 v236, v236
	v_sub_f32_e32 v236, 1.0, v236
	v_fmac_f32_e32 v73, s35, v236
	v_bfe_u32 v236, v235, 18, 1
	v_cvt_f32_u32_e32 v236, v236
	v_sub_f32_e32 v236, 1.0, v236
	v_fmac_f32_e32 v74, s35, v236
	v_bfe_u32 v236, v235, 19, 1
	v_cvt_f32_u32_e32 v236, v236
	v_sub_f32_e32 v236, 1.0, v236
	v_fmac_f32_e32 v75, s35, v236
	v_bfe_u32 v236, v235, 24, 1
	v_cvt_f32_u32_e32 v236, v236
	v_sub_f32_e32 v236, 1.0, v236
	v_fmac_f32_e32 v76, s35, v236
	v_bfe_u32 v236, v235, 25, 1
	v_cvt_f32_u32_e32 v236, v236
	v_sub_f32_e32 v236, 1.0, v236
	v_fmac_f32_e32 v77, s35, v236
	v_bfe_u32 v236, v235, 26, 1
	v_cvt_f32_u32_e32 v236, v236
	v_sub_f32_e32 v236, 1.0, v236
	v_fmac_f32_e32 v78, s35, v236
	v_bfe_u32 v236, v235, 27, 1
	v_cvt_f32_u32_e32 v236, v236
	v_sub_f32_e32 v236, 1.0, v236
	v_fmac_f32_e32 v79, s35, v236

.Lovf_b21:
	s_waitcnt lgkmcnt(0)
	s_nop 15
	s_nop 15
	s_nop 15
	ds_read_b128 v[160:163], v225 offset:23040
	ds_read_b128 v[164:167], v225 offset:23072
	s_waitcnt lgkmcnt(0)
	v_mfma_f32_32x32x16_f16 v[80:95], v[160:163], v[144:147], v[112:127]
	v_mfma_f32_32x32x16_f16 v[80:95], v[164:167], v[148:151], v[80:95]
	s_nop 15
	ds_read_b128 v[160:163], v225 offset:23104
	ds_read_b128 v[164:167], v225 offset:23136
	s_waitcnt lgkmcnt(0)
	v_mfma_f32_32x32x16_f16 v[80:95], v[160:163], v[152:155], v[80:95]
	v_mfma_f32_32x32x16_f16 v[80:95], v[164:167], v[156:159], v[80:95]
	s_nop 15
	s_nop 15
	s_cmp_eq_u64 s[20:21], -1
	s_cbranch_scc1 .Lovfnm_b21
	v_lshrrev_b32_e64 v235, v234, s21
	v_bfe_u32 v236, v235, 0, 1
	v_cvt_f32_u32_e32 v236, v236
	v_sub_f32_e32 v236, 1.0, v236
	v_fmac_f32_e32 v80, s35, v236
	v_bfe_u32 v236, v235, 1, 1
	v_cvt_f32_u32_e32 v236, v236
	v_sub_f32_e32 v236, 1.0, v236
	v_fmac_f32_e32 v81, s35, v236
	v_bfe_u32 v236, v235, 2, 1
	v_cvt_f32_u32_e32 v236, v236
	v_sub_f32_e32 v236, 1.0, v236
	v_fmac_f32_e32 v82, s35, v236
	v_bfe_u32 v236, v235, 3, 1
	v_cvt_f32_u32_e32 v236, v236
	v_sub_f32_e32 v236, 1.0, v236
	v_fmac_f32_e32 v83, s35, v236
	v_bfe_u32 v236, v235, 8, 1
	v_cvt_f32_u32_e32 v236, v236
	v_sub_f32_e32 v236, 1.0, v236
	v_fmac_f32_e32 v84, s35, v236
	v_bfe_u32 v236, v235, 9, 1
	v_cvt_f32_u32_e32 v236, v236
	v_sub_f32_e32 v236, 1.0, v236
	v_fmac_f32_e32 v85, s35, v236
	v_bfe_u32 v236, v235, 10, 1
	v_cvt_f32_u32_e32 v236, v236
	v_sub_f32_e32 v236, 1.0, v236
	v_fmac_f32_e32 v86, s35, v236
	v_bfe_u32 v236, v235, 11, 1
	v_cvt_f32_u32_e32 v236, v236
	v_sub_f32_e32 v236, 1.0, v236
	v_fmac_f32_e32 v87, s35, v236
	v_bfe_u32 v236, v235, 16, 1
	v_cvt_f32_u32_e32 v236, v236
	v_sub_f32_e32 v236, 1.0, v236
	v_fmac_f32_e32 v88, s35, v236
	v_bfe_u32 v236, v235, 17, 1
	v_cvt_f32_u32_e32 v236, v236
	v_sub_f32_e32 v236, 1.0, v236
	v_fmac_f32_e32 v89, s35, v236
	v_bfe_u32 v236, v235, 18, 1
	v_cvt_f32_u32_e32 v236, v236
	v_sub_f32_e32 v236, 1.0, v236
	v_fmac_f32_e32 v90, s35, v236
	v_bfe_u32 v236, v235, 19, 1
	v_cvt_f32_u32_e32 v236, v236
	v_sub_f32_e32 v236, 1.0, v236
	v_fmac_f32_e32 v91, s35, v236
	v_bfe_u32 v236, v235, 24, 1
	v_cvt_f32_u32_e32 v236, v236
	v_sub_f32_e32 v236, 1.0, v236
	v_fmac_f32_e32 v92, s35, v236
	v_bfe_u32 v236, v235, 25, 1
	v_cvt_f32_u32_e32 v236, v236
	v_sub_f32_e32 v236, 1.0, v236
	v_fmac_f32_e32 v93, s35, v236
	v_bfe_u32 v236, v235, 26, 1
	v_cvt_f32_u32_e32 v236, v236
	v_sub_f32_e32 v236, 1.0, v236
	v_fmac_f32_e32 v94, s35, v236
	v_bfe_u32 v236, v235, 27, 1
	v_cvt_f32_u32_e32 v236, v236
	v_sub_f32_e32 v236, 1.0, v236
	v_fmac_f32_e32 v95, s35, v236

.Lovf_a30:
	s_waitcnt lgkmcnt(0)
	s_nop 15
	s_nop 15
	s_nop 15
	ds_read_b128 v[168:171], v225 offset:27648
	ds_read_b128 v[172:175], v225 offset:27680
	s_waitcnt lgkmcnt(0)
	v_mfma_f32_32x32x16_f16 v[64:79], v[168:171], v[128:131], v[96:111]
	v_mfma_f32_32x32x16_f16 v[64:79], v[172:175], v[132:135], v[64:79]
	s_nop 15
	ds_read_b128 v[168:171], v225 offset:27712
	ds_read_b128 v[172:175], v225 offset:27744
	s_waitcnt lgkmcnt(0)
	v_mfma_f32_32x32x16_f16 v[64:79], v[168:171], v[136:139], v[64:79]
	v_mfma_f32_32x32x16_f16 v[64:79], v[172:175], v[140:143], v[64:79]
	s_nop 15
	s_nop 15
	s_cmp_eq_u64 s[20:21], -1
	s_cbranch_scc1 .Lovfnm_a30
	v_lshrrev_b32_e64 v235, v234, s20
	v_bfe_u32 v236, v235, 0, 1
	v_cvt_f32_u32_e32 v236, v236
	v_sub_f32_e32 v236, 1.0, v236
	v_fmac_f32_e32 v64, s35, v236
	v_bfe_u32 v236, v235, 1, 1
	v_cvt_f32_u32_e32 v236, v236
	v_sub_f32_e32 v236, 1.0, v236
	v_fmac_f32_e32 v65, s35, v236
	v_bfe_u32 v236, v235, 2, 1
	v_cvt_f32_u32_e32 v236, v236
	v_sub_f32_e32 v236, 1.0, v236
	v_fmac_f32_e32 v66, s35, v236
	v_bfe_u32 v236, v235, 3, 1
	v_cvt_f32_u32_e32 v236, v236
	v_sub_f32_e32 v236, 1.0, v236
	v_fmac_f32_e32 v67, s35, v236
	v_bfe_u32 v236, v235, 8, 1
	v_cvt_f32_u32_e32 v236, v236
	v_sub_f32_e32 v236, 1.0, v236
	v_fmac_f32_e32 v68, s35, v236
	v_bfe_u32 v236, v235, 9, 1
	v_cvt_f32_u32_e32 v236, v236
	v_sub_f32_e32 v236, 1.0, v236
	v_fmac_f32_e32 v69, s35, v236
	v_bfe_u32 v236, v235, 10, 1
	v_cvt_f32_u32_e32 v236, v236
	v_sub_f32_e32 v236, 1.0, v236
	v_fmac_f32_e32 v70, s35, v236
	v_bfe_u32 v236, v235, 11, 1
	v_cvt_f32_u32_e32 v236, v236
	v_sub_f32_e32 v236, 1.0, v236
	v_fmac_f32_e32 v71, s35, v236
	v_bfe_u32 v236, v235, 16, 1
	v_cvt_f32_u32_e32 v236, v236
	v_sub_f32_e32 v236, 1.0, v236
	v_fmac_f32_e32 v72, s35, v236
	v_bfe_u32 v236, v235, 17, 1
	v_cvt_f32_u32_e32 v236, v236
	v_sub_f32_e32 v236, 1.0, v236
	v_fmac_f32_e32 v73, s35, v236
	v_bfe_u32 v236, v235, 18, 1
	v_cvt_f32_u32_e32 v236, v236
	v_sub_f32_e32 v236, 1.0, v236
	v_fmac_f32_e32 v74, s35, v236
	v_bfe_u32 v236, v235, 19, 1
	v_cvt_f32_u32_e32 v236, v236
	v_sub_f32_e32 v236, 1.0, v236
	v_fmac_f32_e32 v75, s35, v236
	v_bfe_u32 v236, v235, 24, 1
	v_cvt_f32_u32_e32 v236, v236
	v_sub_f32_e32 v236, 1.0, v236
	v_fmac_f32_e32 v76, s35, v236
	v_bfe_u32 v236, v235, 25, 1
	v_cvt_f32_u32_e32 v236, v236
	v_sub_f32_e32 v236, 1.0, v236
	v_fmac_f32_e32 v77, s35, v236
	v_bfe_u32 v236, v235, 26, 1
	v_cvt_f32_u32_e32 v236, v236
	v_sub_f32_e32 v236, 1.0, v236
	v_fmac_f32_e32 v78, s35, v236
	v_bfe_u32 v236, v235, 27, 1
	v_cvt_f32_u32_e32 v236, v236
	v_sub_f32_e32 v236, 1.0, v236
	v_fmac_f32_e32 v79, s35, v236

.Lovf_b30:
	s_waitcnt lgkmcnt(0)
	s_nop 15
	s_nop 15
	s_nop 15
	ds_read_b128 v[160:163], v225 offset:27648
	ds_read_b128 v[164:167], v225 offset:27680
	s_waitcnt lgkmcnt(0)
	v_mfma_f32_32x32x16_f16 v[80:95], v[160:163], v[144:147], v[112:127]
	v_mfma_f32_32x32x16_f16 v[80:95], v[164:167], v[148:151], v[80:95]
	s_nop 15
	ds_read_b128 v[160:163], v225 offset:27712
	ds_read_b128 v[164:167], v225 offset:27744
	s_waitcnt lgkmcnt(0)
	v_mfma_f32_32x32x16_f16 v[80:95], v[160:163], v[152:155], v[80:95]
	v_mfma_f32_32x32x16_f16 v[80:95], v[164:167], v[156:159], v[80:95]
	s_nop 15
	s_nop 15
	s_cmp_eq_u64 s[20:21], -1
	s_cbranch_scc1 .Lovfnm_b30
	v_lshrrev_b32_e64 v235, v234, s20
	v_bfe_u32 v236, v235, 0, 1
	v_cvt_f32_u32_e32 v236, v236
	v_sub_f32_e32 v236, 1.0, v236
	v_fmac_f32_e32 v80, s35, v236
	v_bfe_u32 v236, v235, 1, 1
	v_cvt_f32_u32_e32 v236, v236
	v_sub_f32_e32 v236, 1.0, v236
	v_fmac_f32_e32 v81, s35, v236
	v_bfe_u32 v236, v235, 2, 1
	v_cvt_f32_u32_e32 v236, v236
	v_sub_f32_e32 v236, 1.0, v236
	v_fmac_f32_e32 v82, s35, v236
	v_bfe_u32 v236, v235, 3, 1
	v_cvt_f32_u32_e32 v236, v236
	v_sub_f32_e32 v236, 1.0, v236
	v_fmac_f32_e32 v83, s35, v236
	v_bfe_u32 v236, v235, 8, 1
	v_cvt_f32_u32_e32 v236, v236
	v_sub_f32_e32 v236, 1.0, v236
	v_fmac_f32_e32 v84, s35, v236
	v_bfe_u32 v236, v235, 9, 1
	v_cvt_f32_u32_e32 v236, v236
	v_sub_f32_e32 v236, 1.0, v236
	v_fmac_f32_e32 v85, s35, v236
	v_bfe_u32 v236, v235, 10, 1
	v_cvt_f32_u32_e32 v236, v236
	v_sub_f32_e32 v236, 1.0, v236
	v_fmac_f32_e32 v86, s35, v236
	v_bfe_u32 v236, v235, 11, 1
	v_cvt_f32_u32_e32 v236, v236
	v_sub_f32_e32 v236, 1.0, v236
	v_fmac_f32_e32 v87, s35, v236
	v_bfe_u32 v236, v235, 16, 1
	v_cvt_f32_u32_e32 v236, v236
	v_sub_f32_e32 v236, 1.0, v236
	v_fmac_f32_e32 v88, s35, v236
	v_bfe_u32 v236, v235, 17, 1
	v_cvt_f32_u32_e32 v236, v236
	v_sub_f32_e32 v236, 1.0, v236
	v_fmac_f32_e32 v89, s35, v236
	v_bfe_u32 v236, v235, 18, 1
	v_cvt_f32_u32_e32 v236, v236
	v_sub_f32_e32 v236, 1.0, v236
	v_fmac_f32_e32 v90, s35, v236
	v_bfe_u32 v236, v235, 19, 1
	v_cvt_f32_u32_e32 v236, v236
	v_sub_f32_e32 v236, 1.0, v236
	v_fmac_f32_e32 v91, s35, v236
	v_bfe_u32 v236, v235, 24, 1
	v_cvt_f32_u32_e32 v236, v236
	v_sub_f32_e32 v236, 1.0, v236
	v_fmac_f32_e32 v92, s35, v236
	v_bfe_u32 v236, v235, 25, 1
	v_cvt_f32_u32_e32 v236, v236
	v_sub_f32_e32 v236, 1.0, v236
	v_fmac_f32_e32 v93, s35, v236
	v_bfe_u32 v236, v235, 26, 1
	v_cvt_f32_u32_e32 v236, v236
	v_sub_f32_e32 v236, 1.0, v236
	v_fmac_f32_e32 v94, s35, v236
	v_bfe_u32 v236, v235, 27, 1
	v_cvt_f32_u32_e32 v236, v236
	v_sub_f32_e32 v236, 1.0, v236
	v_fmac_f32_e32 v95, s35, v236

.Lovf_a31:
	s_waitcnt lgkmcnt(0)
	s_nop 15
	s_nop 15
	s_nop 15
	ds_read_b128 v[168:171], v225 offset:32256
	ds_read_b128 v[172:175], v225 offset:32288
	s_waitcnt lgkmcnt(0)
	v_mfma_f32_32x32x16_f16 v[64:79], v[168:171], v[128:131], v[96:111]
	v_mfma_f32_32x32x16_f16 v[64:79], v[172:175], v[132:135], v[64:79]
	s_nop 15
	ds_read_b128 v[168:171], v225 offset:32320
	ds_read_b128 v[172:175], v225 offset:32352
	s_waitcnt lgkmcnt(0)
	v_mfma_f32_32x32x16_f16 v[64:79], v[168:171], v[136:139], v[64:79]
	v_mfma_f32_32x32x16_f16 v[64:79], v[172:175], v[140:143], v[64:79]
	s_nop 15
	s_nop 15
	s_cmp_eq_u64 s[20:21], -1
	s_cbranch_scc1 .Lovfnm_a31
	v_lshrrev_b32_e64 v235, v234, s21
	v_bfe_u32 v236, v235, 0, 1
	v_cvt_f32_u32_e32 v236, v236
	v_sub_f32_e32 v236, 1.0, v236
	v_fmac_f32_e32 v64, s35, v236
	v_bfe_u32 v236, v235, 1, 1
	v_cvt_f32_u32_e32 v236, v236
	v_sub_f32_e32 v236, 1.0, v236
	v_fmac_f32_e32 v65, s35, v236
	v_bfe_u32 v236, v235, 2, 1
	v_cvt_f32_u32_e32 v236, v236
	v_sub_f32_e32 v236, 1.0, v236
	v_fmac_f32_e32 v66, s35, v236
	v_bfe_u32 v236, v235, 3, 1
	v_cvt_f32_u32_e32 v236, v236
	v_sub_f32_e32 v236, 1.0, v236
	v_fmac_f32_e32 v67, s35, v236
	v_bfe_u32 v236, v235, 8, 1
	v_cvt_f32_u32_e32 v236, v236
	v_sub_f32_e32 v236, 1.0, v236
	v_fmac_f32_e32 v68, s35, v236
	v_bfe_u32 v236, v235, 9, 1
	v_cvt_f32_u32_e32 v236, v236
	v_sub_f32_e32 v236, 1.0, v236
	v_fmac_f32_e32 v69, s35, v236
	v_bfe_u32 v236, v235, 10, 1
	v_cvt_f32_u32_e32 v236, v236
	v_sub_f32_e32 v236, 1.0, v236
	v_fmac_f32_e32 v70, s35, v236
	v_bfe_u32 v236, v235, 11, 1
	v_cvt_f32_u32_e32 v236, v236
	v_sub_f32_e32 v236, 1.0, v236
	v_fmac_f32_e32 v71, s35, v236
	v_bfe_u32 v236, v235, 16, 1
	v_cvt_f32_u32_e32 v236, v236
	v_sub_f32_e32 v236, 1.0, v236
	v_fmac_f32_e32 v72, s35, v236
	v_bfe_u32 v236, v235, 17, 1
	v_cvt_f32_u32_e32 v236, v236
	v_sub_f32_e32 v236, 1.0, v236
	v_fmac_f32_e32 v73, s35, v236
	v_bfe_u32 v236, v235, 18, 1
	v_cvt_f32_u32_e32 v236, v236
	v_sub_f32_e32 v236, 1.0, v236
	v_fmac_f32_e32 v74, s35, v236
	v_bfe_u32 v236, v235, 19, 1
	v_cvt_f32_u32_e32 v236, v236
	v_sub_f32_e32 v236, 1.0, v236
	v_fmac_f32_e32 v75, s35, v236
	v_bfe_u32 v236, v235, 24, 1
	v_cvt_f32_u32_e32 v236, v236
	v_sub_f32_e32 v236, 1.0, v236
	v_fmac_f32_e32 v76, s35, v236
	v_bfe_u32 v236, v235, 25, 1
	v_cvt_f32_u32_e32 v236, v236
	v_sub_f32_e32 v236, 1.0, v236
	v_fmac_f32_e32 v77, s35, v236
	v_bfe_u32 v236, v235, 26, 1
	v_cvt_f32_u32_e32 v236, v236
	v_sub_f32_e32 v236, 1.0, v236
	v_fmac_f32_e32 v78, s35, v236
	v_bfe_u32 v236, v235, 27, 1
	v_cvt_f32_u32_e32 v236, v236
	v_sub_f32_e32 v236, 1.0, v236
	v_fmac_f32_e32 v79, s35, v236

.Lovf_b31:
	s_waitcnt lgkmcnt(0)
	s_nop 15
	s_nop 15
	s_nop 15
	ds_read_b128 v[160:163], v225 offset:32256
	ds_read_b128 v[164:167], v225 offset:32288
	s_waitcnt lgkmcnt(0)
	v_mfma_f32_32x32x16_f16 v[80:95], v[160:163], v[144:147], v[112:127]
	v_mfma_f32_32x32x16_f16 v[80:95], v[164:167], v[148:151], v[80:95]
	s_nop 15
	ds_read_b128 v[160:163], v225 offset:32320
	ds_read_b128 v[164:167], v225 offset:32352
	s_waitcnt lgkmcnt(0)
	v_mfma_f32_32x32x16_f16 v[80:95], v[160:163], v[152:155], v[80:95]
	v_mfma_f32_32x32x16_f16 v[80:95], v[164:167], v[156:159], v[80:95]
	s_nop 15
	s_nop 15
	s_cmp_eq_u64 s[20:21], -1
	s_cbranch_scc1 .Lovfnm_b31
	v_lshrrev_b32_e64 v235, v234, s21
	v_bfe_u32 v236, v235, 0, 1
	v_cvt_f32_u32_e32 v236, v236
	v_sub_f32_e32 v236, 1.0, v236
	v_fmac_f32_e32 v80, s35, v236
	v_bfe_u32 v236, v235, 1, 1
	v_cvt_f32_u32_e32 v236, v236
	v_sub_f32_e32 v236, 1.0, v236
	v_fmac_f32_e32 v81, s35, v236
	v_bfe_u32 v236, v235, 2, 1
	v_cvt_f32_u32_e32 v236, v236
	v_sub_f32_e32 v236, 1.0, v236
	v_fmac_f32_e32 v82, s35, v236
	v_bfe_u32 v236, v235, 3, 1
	v_cvt_f32_u32_e32 v236, v236
	v_sub_f32_e32 v236, 1.0, v236
	v_fmac_f32_e32 v83, s35, v236
	v_bfe_u32 v236, v235, 8, 1
	v_cvt_f32_u32_e32 v236, v236
	v_sub_f32_e32 v236, 1.0, v236
	v_fmac_f32_e32 v84, s35, v236
	v_bfe_u32 v236, v235, 9, 1
	v_cvt_f32_u32_e32 v236, v236
	v_sub_f32_e32 v236, 1.0, v236
	v_fmac_f32_e32 v85, s35, v236
	v_bfe_u32 v236, v235, 10, 1
	v_cvt_f32_u32_e32 v236, v236
	v_sub_f32_e32 v236, 1.0, v236
	v_fmac_f32_e32 v86, s35, v236
	v_bfe_u32 v236, v235, 11, 1
	v_cvt_f32_u32_e32 v236, v236
	v_sub_f32_e32 v236, 1.0, v236
	v_fmac_f32_e32 v87, s35, v236
	v_bfe_u32 v236, v235, 16, 1
	v_cvt_f32_u32_e32 v236, v236
	v_sub_f32_e32 v236, 1.0, v236
	v_fmac_f32_e32 v88, s35, v236
	v_bfe_u32 v236, v235, 17, 1
	v_cvt_f32_u32_e32 v236, v236
	v_sub_f32_e32 v236, 1.0, v236
	v_fmac_f32_e32 v89, s35, v236
	v_bfe_u32 v236, v235, 18, 1
	v_cvt_f32_u32_e32 v236, v236
	v_sub_f32_e32 v236, 1.0, v236
	v_fmac_f32_e32 v90, s35, v236
	v_bfe_u32 v236, v235, 19, 1
	v_cvt_f32_u32_e32 v236, v236
	v_sub_f32_e32 v236, 1.0, v236
	v_fmac_f32_e32 v91, s35, v236
	v_bfe_u32 v236, v235, 24, 1
	v_cvt_f32_u32_e32 v236, v236
	v_sub_f32_e32 v236, 1.0, v236
	v_fmac_f32_e32 v92, s35, v236
	v_bfe_u32 v236, v235, 25, 1
	v_cvt_f32_u32_e32 v236, v236
	v_sub_f32_e32 v236, 1.0, v236
	v_fmac_f32_e32 v93, s35, v236
	v_bfe_u32 v236, v235, 26, 1
	v_cvt_f32_u32_e32 v236, v236
	v_sub_f32_e32 v236, 1.0, v236
	v_fmac_f32_e32 v94, s35, v236
	v_bfe_u32 v236, v235, 27, 1
	v_cvt_f32_u32_e32 v236, v236
	v_sub_f32_e32 v236, 1.0, v236
	v_fmac_f32_e32 v95, s35, v236

	.amdhsa_kernel _Z8attn_fwdPKfPKiPf
		.amdhsa_group_segment_fixed_size 143360
		.amdhsa_private_segment_fixed_size 0
		.amdhsa_kernarg_size 24
		.amdhsa_user_sgpr_count 2
		.amdhsa_user_sgpr_dispatch_ptr 0
		.amdhsa_user_sgpr_queue_ptr 0
		.amdhsa_user_sgpr_kernarg_segment_ptr 1
		.amdhsa_user_sgpr_dispatch_id 0
		.amdhsa_user_sgpr_kernarg_preload_length 0
		.amdhsa_user_sgpr_kernarg_preload_offset 0
		.amdhsa_user_sgpr_private_segment_size 0
		.amdhsa_uses_dynamic_stack 0
		.amdhsa_enable_private_segment 0
		.amdhsa_system_sgpr_workgroup_id_x 1
		.amdhsa_system_sgpr_workgroup_id_y 0
		.amdhsa_system_sgpr_workgroup_id_z 0
		.amdhsa_system_sgpr_workgroup_info 0
		.amdhsa_system_vgpr_workitem_id 0
		.amdhsa_next_free_vgpr 248
		.amdhsa_next_free_sgpr 48
		.amdhsa_accum_offset 248
		.amdhsa_reserve_vcc 1
		.amdhsa_float_round_mode_32 0
		.amdhsa_float_round_mode_16_64 0
		.amdhsa_float_denorm_mode_32 3
		.amdhsa_float_denorm_mode_16_64 3
		.amdhsa_dx10_clamp 1
		.amdhsa_ieee_mode 1
		.amdhsa_fp16_overflow 0
		.amdhsa_tg_split 0
		.amdhsa_exception_fp_ieee_invalid_op 0
		.amdhsa_exception_fp_denorm_src 0
		.amdhsa_exception_fp_ieee_div_zero 0
		.amdhsa_exception_fp_ieee_overflow 0
		.amdhsa_exception_fp_ieee_underflow 0
		.amdhsa_exception_fp_ieee_inexact 0
		.amdhsa_exception_int_div_zero 0
	.end_amdhsa_kernel

.Lfunc_end0:
	.size	_Z8attn_fwdPKfPKiPf, .Lfunc_end0-_Z8attn_fwdPKfPKiPf
	.set _Z8attn_fwdPKfPKiPf.num_vgpr, 248
	.set _Z8attn_fwdPKfPKiPf.num_agpr, 0
	.set _Z8attn_fwdPKfPKiPf.numbered_sgpr, 48
	.set _Z8attn_fwdPKfPKiPf.num_named_barrier, 0
	.set _Z8attn_fwdPKfPKiPf.private_seg_size, 0
	.set _Z8attn_fwdPKfPKiPf.uses_vcc, 1
	.set _Z8attn_fwdPKfPKiPf.uses_flat_scratch, 0
	.set _Z8attn_fwdPKfPKiPf.has_dyn_sized_stack, 0
	.set _Z8attn_fwdPKfPKiPf.has_recursion, 0
	.set _Z8attn_fwdPKfPKiPf.has_indirect_call, 0

amdhsa.kernels:
  - .agpr_count:     0
    .args:
      - .actual_access:  read_only
        .address_space:  global
        .offset:         0
        .size:           8
        .value_kind:     global_buffer
      - .actual_access:  read_only
        .address_space:  global
        .offset:         8
        .size:           8
        .value_kind:     global_buffer
      - .actual_access:  write_only
        .address_space:  global
        .offset:         16
        .size:           8
        .value_kind:     global_buffer
    .group_segment_fixed_size: 143360
    .kernarg_segment_align: 8
    .kernarg_segment_size: 24
    .language:       OpenCL C
    .language_version:
      - 2
      - 0
    .max_flat_workgroup_size: 512
    .name:           _Z8attn_fwdPKfPKiPf
    .private_segment_fixed_size: 0
    .sgpr_count:     54
    .sgpr_spill_count: 0
    .symbol:         _Z8attn_fwdPKfPKiPf.kd
    .uniform_work_group_size: 1
    .uses_dynamic_stack: false
    .vgpr_count:     248
    .vgpr_spill_count: 0
    .wavefront_size: 64
